# P1 epilogue stores carry the nt hint (write-once outputs)
# speedup vs baseline: 1.0112x; 1.0112x over previous
.LBB0_187:
	s_or_b64 exec, exec, s[6:7]
	v_lshlrev_b64 v[224:225], 7, v[206:207]
	v_ashrrev_i32_e32 v223, 31, v222
	v_lshl_add_u64 v[224:225], s[12:13], 0, v[224:225]
	v_lshl_add_u64 v[224:225], v[222:223], 2, v[224:225]
	global_store_dwordx4 v[224:225], v[2:5], off nt
	global_store_dwordx4 v[224:225], v[6:9], off offset:16 nt
	s_and_saveexec_b64 s[6:7], s[4:5]
	s_xor_b64 s[6:7], exec, s[6:7]
	s_cbranch_execz .LBB0_189
	v_mul_f32_e32 v2, 0xbfb8aa3b, v134
	v_mul_f32_e32 v3, 0xbfb8aa3b, v135
	v_mul_f32_e32 v4, 0xbfb8aa3b, v136
	v_mul_f32_e32 v5, 0xbfb8aa3b, v137
	v_mul_f32_e32 v6, 0xbfb8aa3b, v146
	v_mul_f32_e32 v7, 0xbfb8aa3b, v147
	v_mul_f32_e32 v8, 0xbfb8aa3b, v148
	v_mul_f32_e32 v9, 0xbfb8aa3b, v149
	v_exp_f32_e32 v2, v2
	v_exp_f32_e32 v3, v3
	v_exp_f32_e32 v4, v4
	v_exp_f32_e32 v5, v5
	v_exp_f32_e32 v6, v6
	v_exp_f32_e32 v7, v7
	v_exp_f32_e32 v8, v8
	v_exp_f32_e32 v9, v9
	v_add_f32_e32 v2, 1.0, v2
	v_add_f32_e32 v3, 1.0, v3
	v_add_f32_e32 v4, 1.0, v4
	v_add_f32_e32 v5, 1.0, v5
	v_add_f32_e32 v6, 1.0, v6
	v_add_f32_e32 v7, 1.0, v7
	v_add_f32_e32 v8, 1.0, v8
	v_add_f32_e32 v9, 1.0, v9
	v_rcp_f32_e32 v2, v2
	v_rcp_f32_e32 v3, v3
	v_rcp_f32_e32 v4, v4
	v_rcp_f32_e32 v5, v5
	v_rcp_f32_e32 v6, v6
	v_rcp_f32_e32 v7, v7
	v_rcp_f32_e32 v8, v8
	v_rcp_f32_e32 v9, v9

.LBB0_191:
	s_or_b64 exec, exec, s[6:7]
	v_lshlrev_b64 v[224:225], 7, v[208:209]
	v_lshl_add_u64 v[224:225], s[12:13], 0, v[224:225]
	v_lshl_add_u64 v[224:225], v[222:223], 2, v[224:225]
	global_store_dwordx4 v[224:225], v[2:5], off nt
	global_store_dwordx4 v[224:225], v[6:9], off offset:16 nt
	s_and_saveexec_b64 s[6:7], s[4:5]
	s_xor_b64 s[6:7], exec, s[6:7]
	s_cbranch_execz .LBB0_193
	v_mul_f32_e32 v2, 0xbfb8aa3b, v158
	v_mul_f32_e32 v3, 0xbfb8aa3b, v159
	v_mul_f32_e32 v4, 0xbfb8aa3b, v160
	v_mul_f32_e32 v5, 0xbfb8aa3b, v161
	v_mul_f32_e32 v6, 0xbfb8aa3b, v114
	v_mul_f32_e32 v7, 0xbfb8aa3b, v115
	v_mul_f32_e32 v8, 0xbfb8aa3b, v116
	v_mul_f32_e32 v9, 0xbfb8aa3b, v117
	v_exp_f32_e32 v2, v2
	v_exp_f32_e32 v3, v3
	v_exp_f32_e32 v4, v4
	v_exp_f32_e32 v5, v5
	v_exp_f32_e32 v6, v6
	v_exp_f32_e32 v7, v7
	v_exp_f32_e32 v8, v8
	v_exp_f32_e32 v9, v9
	v_add_f32_e32 v2, 1.0, v2
	v_add_f32_e32 v3, 1.0, v3
	v_add_f32_e32 v4, 1.0, v4
	v_add_f32_e32 v5, 1.0, v5
	v_add_f32_e32 v6, 1.0, v6
	v_add_f32_e32 v7, 1.0, v7
	v_add_f32_e32 v8, 1.0, v8
	v_add_f32_e32 v9, 1.0, v9
	v_rcp_f32_e32 v2, v2
	v_rcp_f32_e32 v3, v3
	v_rcp_f32_e32 v4, v4
	v_rcp_f32_e32 v5, v5
	v_rcp_f32_e32 v6, v6
	v_rcp_f32_e32 v7, v7
	v_rcp_f32_e32 v8, v8
	v_rcp_f32_e32 v9, v9

.LBB0_195:
	s_or_b64 exec, exec, s[6:7]
	v_lshlrev_b64 v[224:225], 7, v[210:211]
	v_lshl_add_u64 v[224:225], s[12:13], 0, v[224:225]
	v_lshl_add_u64 v[224:225], v[222:223], 2, v[224:225]
	global_store_dwordx4 v[224:225], v[2:5], off nt
	global_store_dwordx4 v[224:225], v[6:9], off offset:16 nt
	s_and_saveexec_b64 s[6:7], s[4:5]
	s_xor_b64 s[6:7], exec, s[6:7]
	s_cbranch_execz .LBB0_197
	v_mul_f32_e32 v2, 0xbfb8aa3b, v126
	v_mul_f32_e32 v3, 0xbfb8aa3b, v127
	v_mul_f32_e32 v4, 0xbfb8aa3b, v128
	v_mul_f32_e32 v5, 0xbfb8aa3b, v129
	v_mul_f32_e32 v6, 0xbfb8aa3b, v138
	v_mul_f32_e32 v7, 0xbfb8aa3b, v139
	v_mul_f32_e32 v8, 0xbfb8aa3b, v140
	v_mul_f32_e32 v9, 0xbfb8aa3b, v141
	v_exp_f32_e32 v2, v2
	v_exp_f32_e32 v3, v3
	v_exp_f32_e32 v4, v4
	v_exp_f32_e32 v5, v5
	v_exp_f32_e32 v6, v6
	v_exp_f32_e32 v7, v7
	v_exp_f32_e32 v8, v8
	v_exp_f32_e32 v9, v9
	v_add_f32_e32 v2, 1.0, v2
	v_add_f32_e32 v3, 1.0, v3
	v_add_f32_e32 v4, 1.0, v4
	v_add_f32_e32 v5, 1.0, v5
	v_add_f32_e32 v6, 1.0, v6
	v_add_f32_e32 v7, 1.0, v7
	v_add_f32_e32 v8, 1.0, v8
	v_add_f32_e32 v9, 1.0, v9
	v_rcp_f32_e32 v2, v2
	v_rcp_f32_e32 v3, v3
	v_rcp_f32_e32 v4, v4
	v_rcp_f32_e32 v5, v5
	v_rcp_f32_e32 v6, v6
	v_rcp_f32_e32 v7, v7
	v_rcp_f32_e32 v8, v8
	v_rcp_f32_e32 v9, v9

.LBB0_199:
	s_or_b64 exec, exec, s[6:7]
	v_lshlrev_b64 v[224:225], 7, v[212:213]
	v_lshl_add_u64 v[224:225], s[12:13], 0, v[224:225]
	v_lshl_add_u64 v[224:225], v[222:223], 2, v[224:225]
	global_store_dwordx4 v[224:225], v[2:5], off nt
	global_store_dwordx4 v[224:225], v[6:9], off offset:16 nt
	s_and_saveexec_b64 s[6:7], s[4:5]
	s_xor_b64 s[6:7], exec, s[6:7]
	s_cbranch_execz .LBB0_201
	v_mul_f32_e32 v2, 0xbfb8aa3b, v66
	v_mul_f32_e32 v3, 0xbfb8aa3b, v67
	v_mul_f32_e32 v4, 0xbfb8aa3b, v68
	v_mul_f32_e32 v5, 0xbfb8aa3b, v69
	v_mul_f32_e32 v6, 0xbfb8aa3b, v70
	v_mul_f32_e32 v7, 0xbfb8aa3b, v71
	v_mul_f32_e32 v8, 0xbfb8aa3b, v72
	v_mul_f32_e32 v9, 0xbfb8aa3b, v73
	v_exp_f32_e32 v2, v2
	v_exp_f32_e32 v3, v3
	v_exp_f32_e32 v4, v4
	v_exp_f32_e32 v5, v5
	v_exp_f32_e32 v6, v6
	v_exp_f32_e32 v7, v7
	v_exp_f32_e32 v8, v8
	v_exp_f32_e32 v9, v9
	v_add_f32_e32 v2, 1.0, v2
	v_add_f32_e32 v3, 1.0, v3
	v_add_f32_e32 v4, 1.0, v4
	v_add_f32_e32 v5, 1.0, v5
	v_add_f32_e32 v6, 1.0, v6
	v_add_f32_e32 v7, 1.0, v7
	v_add_f32_e32 v8, 1.0, v8
	v_add_f32_e32 v9, 1.0, v9
	v_rcp_f32_e32 v2, v2
	v_rcp_f32_e32 v3, v3
	v_rcp_f32_e32 v4, v4
	v_rcp_f32_e32 v5, v5
	v_rcp_f32_e32 v6, v6
	v_rcp_f32_e32 v7, v7
	v_rcp_f32_e32 v8, v8
	v_rcp_f32_e32 v9, v9

.LBB0_203:
	s_or_b64 exec, exec, s[6:7]
	v_lshlrev_b64 v[224:225], 7, v[214:215]
	v_lshl_add_u64 v[224:225], s[12:13], 0, v[224:225]
	v_lshl_add_u64 v[224:225], v[222:223], 2, v[224:225]
	global_store_dwordx4 v[224:225], v[2:5], off nt
	global_store_dwordx4 v[224:225], v[6:9], off offset:16 nt
	s_and_saveexec_b64 s[6:7], s[4:5]
	s_xor_b64 s[6:7], exec, s[6:7]
	s_cbranch_execz .LBB0_205
	v_mul_f32_e32 v2, 0xbfb8aa3b, v74
	v_mul_f32_e32 v3, 0xbfb8aa3b, v75
	v_mul_f32_e32 v4, 0xbfb8aa3b, v76
	v_mul_f32_e32 v5, 0xbfb8aa3b, v77
	v_mul_f32_e32 v6, 0xbfb8aa3b, v78
	v_mul_f32_e32 v7, 0xbfb8aa3b, v79
	v_mul_f32_e32 v8, 0xbfb8aa3b, v80
	v_mul_f32_e32 v9, 0xbfb8aa3b, v81
	v_exp_f32_e32 v2, v2
	v_exp_f32_e32 v3, v3
	v_exp_f32_e32 v4, v4
	v_exp_f32_e32 v5, v5
	v_exp_f32_e32 v6, v6
	v_exp_f32_e32 v7, v7
	v_exp_f32_e32 v8, v8
	v_exp_f32_e32 v9, v9
	v_add_f32_e32 v2, 1.0, v2
	v_add_f32_e32 v3, 1.0, v3
	v_add_f32_e32 v4, 1.0, v4
	v_add_f32_e32 v5, 1.0, v5
	v_add_f32_e32 v6, 1.0, v6
	v_add_f32_e32 v7, 1.0, v7
	v_add_f32_e32 v8, 1.0, v8
	v_add_f32_e32 v9, 1.0, v9
	v_rcp_f32_e32 v2, v2
	v_rcp_f32_e32 v3, v3
	v_rcp_f32_e32 v4, v4
	v_rcp_f32_e32 v5, v5
	v_rcp_f32_e32 v6, v6
	v_rcp_f32_e32 v7, v7
	v_rcp_f32_e32 v8, v8
	v_rcp_f32_e32 v9, v9

.LBB0_207:
	s_or_b64 exec, exec, s[6:7]
	v_lshlrev_b64 v[224:225], 7, v[216:217]
	v_lshl_add_u64 v[224:225], s[12:13], 0, v[224:225]
	v_lshl_add_u64 v[224:225], v[222:223], 2, v[224:225]
	global_store_dwordx4 v[224:225], v[2:5], off nt
	global_store_dwordx4 v[224:225], v[6:9], off offset:16 nt
	s_and_saveexec_b64 s[6:7], s[4:5]
	s_xor_b64 s[6:7], exec, s[6:7]
	s_cbranch_execz .LBB0_209
	v_mul_f32_e32 v2, 0xbfb8aa3b, v82
	v_mul_f32_e32 v3, 0xbfb8aa3b, v83
	v_mul_f32_e32 v4, 0xbfb8aa3b, v84
	v_mul_f32_e32 v5, 0xbfb8aa3b, v85
	v_mul_f32_e32 v6, 0xbfb8aa3b, v86
	v_mul_f32_e32 v7, 0xbfb8aa3b, v87
	v_mul_f32_e32 v8, 0xbfb8aa3b, v88
	v_mul_f32_e32 v9, 0xbfb8aa3b, v89
	v_exp_f32_e32 v2, v2
	v_exp_f32_e32 v3, v3
	v_exp_f32_e32 v4, v4
	v_exp_f32_e32 v5, v5
	v_exp_f32_e32 v6, v6
	v_exp_f32_e32 v7, v7
	v_exp_f32_e32 v8, v8
	v_exp_f32_e32 v9, v9
	v_add_f32_e32 v2, 1.0, v2
	v_add_f32_e32 v3, 1.0, v3
	v_add_f32_e32 v4, 1.0, v4
	v_add_f32_e32 v5, 1.0, v5
	v_add_f32_e32 v6, 1.0, v6
	v_add_f32_e32 v7, 1.0, v7
	v_add_f32_e32 v8, 1.0, v8
	v_add_f32_e32 v9, 1.0, v9
	v_rcp_f32_e32 v2, v2
	v_rcp_f32_e32 v3, v3
	v_rcp_f32_e32 v4, v4
	v_rcp_f32_e32 v5, v5
	v_rcp_f32_e32 v6, v6
	v_rcp_f32_e32 v7, v7
	v_rcp_f32_e32 v8, v8
	v_rcp_f32_e32 v9, v9

.LBB0_211:
	s_or_b64 exec, exec, s[6:7]
	v_lshlrev_b64 v[224:225], 7, v[218:219]
	v_lshl_add_u64 v[224:225], s[12:13], 0, v[224:225]
	v_lshl_add_u64 v[224:225], v[222:223], 2, v[224:225]
	global_store_dwordx4 v[224:225], v[2:5], off nt
	global_store_dwordx4 v[224:225], v[6:9], off offset:16 nt
	s_and_saveexec_b64 s[6:7], s[4:5]
	s_xor_b64 s[6:7], exec, s[6:7]
	s_cbranch_execz .LBB0_213
	v_mul_f32_e32 v2, 0xbfb8aa3b, v90
	v_mul_f32_e32 v3, 0xbfb8aa3b, v91
	v_mul_f32_e32 v4, 0xbfb8aa3b, v92
	v_mul_f32_e32 v5, 0xbfb8aa3b, v93
	v_mul_f32_e32 v6, 0xbfb8aa3b, v94
	v_mul_f32_e32 v7, 0xbfb8aa3b, v95
	v_mul_f32_e32 v8, 0xbfb8aa3b, v96
	v_mul_f32_e32 v9, 0xbfb8aa3b, v97
	v_exp_f32_e32 v2, v2
	v_exp_f32_e32 v3, v3
	v_exp_f32_e32 v4, v4
	v_exp_f32_e32 v5, v5
	v_exp_f32_e32 v6, v6
	v_exp_f32_e32 v7, v7
	v_exp_f32_e32 v8, v8
	v_exp_f32_e32 v9, v9
	v_add_f32_e32 v2, 1.0, v2
	v_add_f32_e32 v3, 1.0, v3
	v_add_f32_e32 v4, 1.0, v4
	v_add_f32_e32 v5, 1.0, v5
	v_add_f32_e32 v6, 1.0, v6
	v_add_f32_e32 v7, 1.0, v7
	v_add_f32_e32 v8, 1.0, v8
	v_add_f32_e32 v9, 1.0, v9
	v_rcp_f32_e32 v2, v2
	v_rcp_f32_e32 v3, v3
	v_rcp_f32_e32 v4, v4
	v_rcp_f32_e32 v5, v5
	v_rcp_f32_e32 v6, v6
	v_rcp_f32_e32 v7, v7
	v_rcp_f32_e32 v8, v8
	v_rcp_f32_e32 v9, v9

.LBB0_215:
	s_or_b64 exec, exec, s[6:7]
	s_waitcnt vmcnt(0)
	v_lshlrev_b64 v[10:11], 7, v[220:221]
	v_lshl_add_u64 v[10:11], s[12:13], 0, v[10:11]
	v_lshl_add_u64 v[10:11], v[222:223], 2, v[10:11]
	global_store_dwordx4 v[10:11], v[2:5], off nt
	global_store_dwordx4 v[10:11], v[6:9], off offset:16 nt

.LBB0_217:
	s_andn2_b64 vcc, exec, s[6:7]
	s_cbranch_vccnz .LBB0_219
	v_mul_f32_e32 v8, 0xbfb8aa3b, v122
	v_exp_f32_e32 v8, v8
	v_mul_f32_e32 v9, 0xbfb8aa3b, v123
	v_exp_f32_e32 v9, v9
	v_mul_f32_e32 v4, 0xbfb8aa3b, v106
	v_add_f32_e32 v8, 1.0, v8
	s_waitcnt vmcnt(0)
	v_rcp_f32_e32 v10, v8
	v_add_f32_e32 v8, 1.0, v9
	v_mul_f32_e32 v9, 0xbfb8aa3b, v124
	v_mul_f32_e32 v5, 0xbfb8aa3b, v107
	v_mul_f32_e32 v6, 0xbfb8aa3b, v108
	v_mul_f32_e32 v7, 0xbfb8aa3b, v109
	v_exp_f32_e32 v9, v9
	v_mul_f32_e32 v11, 0xbfb8aa3b, v125
	s_sub_i32 s31, s29, 22
	v_exp_f32_e32 v4, v4
	v_exp_f32_e32 v5, v5
	v_exp_f32_e32 v6, v6
	v_exp_f32_e32 v7, v7
	v_exp_f32_e32 v11, v11
	s_lshr_b32 s8, s31, 3
	s_lshl_b64 s[6:7], s[8:9], 26
	s_add_u32 s6, s80, s6
	v_rcp_f32_e32 v12, v8
	v_add_f32_e32 v8, 1.0, v9
	s_addc_u32 s7, s81, s7
	s_lshl_b32 s8, s31, 8
	v_add_f32_e32 v4, 1.0, v4
	v_add_f32_e32 v5, 1.0, v5
	v_add_f32_e32 v6, 1.0, v6
	v_add_f32_e32 v7, 1.0, v7
	v_rcp_f32_e32 v13, v8
	v_add_f32_e32 v8, 1.0, v11
	s_and_b32 s8, s8, 0x600
	v_mov_b32_e32 v2, v235
	v_mov_b32_e32 v3, v240
	v_rcp_f32_e32 v4, v4
	v_rcp_f32_e32 v5, v5
	v_rcp_f32_e32 v6, v6
	v_rcp_f32_e32 v7, v7
	v_rcp_f32_e32 v11, v8
	s_add_u32 s6, s6, s8
	s_addc_u32 s7, s7, 0
	v_ashrrev_i32_e32 v3, 31, v2
	v_lshl_add_u64 v[2:3], v[2:3], 1, s[6:7]
	v_lshl_add_u64 v[8:9], v[2:3], 0, v[64:65]
	v_cvt_pk_bf16_f32 v4, v4, v5
	v_cvt_pk_bf16_f32 v5, v6, v7
	v_cvt_pk_bf16_f32 v6, v10, v12
	v_cvt_pk_bf16_f32 v7, v13, v11
	global_store_dwordx4 v[8:9], v[4:7], off nt
	v_mul_f32_e32 v8, 0xbfb8aa3b, v146
	v_mul_f32_e32 v10, 0xbfb8aa3b, v134
	v_exp_f32_e32 v8, v8
	v_mul_f32_e32 v9, 0xbfb8aa3b, v147
	v_exp_f32_e32 v10, v10
	v_mul_f32_e32 v11, 0xbfb8aa3b, v135
	v_exp_f32_e32 v9, v9
	v_exp_f32_e32 v11, v11
	v_add_f32_e32 v8, 1.0, v8
	v_add_f32_e32 v4, 1.0, v10
	v_rcp_f32_e32 v10, v8
	v_add_f32_e32 v8, 1.0, v9
	v_mul_f32_e32 v9, 0xbfb8aa3b, v148
	v_add_f32_e32 v5, 1.0, v11
	v_mul_f32_e32 v6, 0xbfb8aa3b, v136
	v_mul_f32_e32 v7, 0xbfb8aa3b, v137
	v_exp_f32_e32 v9, v9
	v_mul_f32_e32 v11, 0xbfb8aa3b, v149
	v_exp_f32_e32 v6, v6
	v_exp_f32_e32 v7, v7
	v_exp_f32_e32 v11, v11
	v_rcp_f32_e32 v12, v8
	v_add_f32_e32 v8, 1.0, v9
	v_add_f32_e32 v6, 1.0, v6
	v_add_f32_e32 v7, 1.0, v7
	v_rcp_f32_e32 v13, v8
	v_add_f32_e32 v8, 1.0, v11
	v_rcp_f32_e32 v4, v4
	v_rcp_f32_e32 v5, v5
	v_rcp_f32_e32 v6, v6
	v_rcp_f32_e32 v7, v7
	v_rcp_f32_e32 v11, v8
	v_lshl_add_u64 v[8:9], v[2:3], 0, v[62:63]
	v_cvt_pk_bf16_f32 v4, v4, v5
	v_cvt_pk_bf16_f32 v5, v6, v7
	v_cvt_pk_bf16_f32 v6, v10, v12
	v_cvt_pk_bf16_f32 v7, v13, v11
	global_store_dwordx4 v[8:9], v[4:7], off nt
	v_mul_f32_e32 v8, 0xbfb8aa3b, v114
	v_mul_f32_e32 v10, 0xbfb8aa3b, v158
	v_exp_f32_e32 v8, v8
	v_mul_f32_e32 v9, 0xbfb8aa3b, v115
	v_exp_f32_e32 v10, v10
	v_mul_f32_e32 v11, 0xbfb8aa3b, v159
	v_exp_f32_e32 v9, v9
	v_exp_f32_e32 v11, v11
	v_add_f32_e32 v8, 1.0, v8
	v_add_f32_e32 v4, 1.0, v10
	v_rcp_f32_e32 v10, v8
	v_add_f32_e32 v8, 1.0, v9
	v_mul_f32_e32 v9, 0xbfb8aa3b, v116
	v_add_f32_e32 v5, 1.0, v11
	v_mul_f32_e32 v6, 0xbfb8aa3b, v160
	v_mul_f32_e32 v7, 0xbfb8aa3b, v161
	v_exp_f32_e32 v9, v9
	v_mul_f32_e32 v11, 0xbfb8aa3b, v117
	v_exp_f32_e32 v6, v6
	v_exp_f32_e32 v7, v7
	v_exp_f32_e32 v11, v11
	v_rcp_f32_e32 v12, v8
	v_add_f32_e32 v8, 1.0, v9
	v_add_f32_e32 v6, 1.0, v6
	v_add_f32_e32 v7, 1.0, v7
	v_rcp_f32_e32 v13, v8
	v_add_f32_e32 v8, 1.0, v11
	v_rcp_f32_e32 v4, v4
	v_rcp_f32_e32 v5, v5
	v_rcp_f32_e32 v6, v6
	v_rcp_f32_e32 v7, v7
	v_rcp_f32_e32 v11, v8
	v_lshl_add_u64 v[8:9], v[2:3], 0, v[60:61]
	v_cvt_pk_bf16_f32 v4, v4, v5
	v_cvt_pk_bf16_f32 v5, v6, v7
	v_cvt_pk_bf16_f32 v6, v10, v12
	v_cvt_pk_bf16_f32 v7, v13, v11
	global_store_dwordx4 v[8:9], v[4:7], off nt
	v_mul_f32_e32 v8, 0xbfb8aa3b, v138
	v_mul_f32_e32 v10, 0xbfb8aa3b, v126
	v_exp_f32_e32 v8, v8
	v_mul_f32_e32 v9, 0xbfb8aa3b, v139
	v_exp_f32_e32 v10, v10
	v_mul_f32_e32 v11, 0xbfb8aa3b, v127
	v_exp_f32_e32 v9, v9
	v_exp_f32_e32 v11, v11
	v_add_f32_e32 v8, 1.0, v8
	v_add_f32_e32 v4, 1.0, v10
	v_rcp_f32_e32 v10, v8
	v_add_f32_e32 v8, 1.0, v9
	v_mul_f32_e32 v9, 0xbfb8aa3b, v140
	v_add_f32_e32 v5, 1.0, v11
	v_mul_f32_e32 v6, 0xbfb8aa3b, v128
	v_mul_f32_e32 v7, 0xbfb8aa3b, v129
	v_exp_f32_e32 v9, v9
	v_mul_f32_e32 v11, 0xbfb8aa3b, v141
	v_exp_f32_e32 v6, v6
	v_exp_f32_e32 v7, v7
	v_exp_f32_e32 v11, v11
	v_rcp_f32_e32 v12, v8
	v_add_f32_e32 v8, 1.0, v9
	v_add_f32_e32 v6, 1.0, v6
	v_add_f32_e32 v7, 1.0, v7
	v_rcp_f32_e32 v13, v8
	v_add_f32_e32 v8, 1.0, v11
	v_rcp_f32_e32 v4, v4
	v_rcp_f32_e32 v5, v5
	v_rcp_f32_e32 v6, v6
	v_rcp_f32_e32 v7, v7
	v_rcp_f32_e32 v11, v8
	v_lshl_add_u64 v[8:9], v[2:3], 0, v[58:59]
	v_cvt_pk_bf16_f32 v4, v4, v5
	v_cvt_pk_bf16_f32 v5, v6, v7
	v_cvt_pk_bf16_f32 v6, v10, v12
	v_cvt_pk_bf16_f32 v7, v13, v11
	global_store_dwordx4 v[8:9], v[4:7], off nt
	v_mul_f32_e32 v8, 0xbfb8aa3b, v70
	v_mul_f32_e32 v10, 0xbfb8aa3b, v66
	v_exp_f32_e32 v8, v8
	v_mul_f32_e32 v9, 0xbfb8aa3b, v71
	v_exp_f32_e32 v10, v10
	v_mul_f32_e32 v11, 0xbfb8aa3b, v67
	v_exp_f32_e32 v9, v9
	v_exp_f32_e32 v11, v11
	v_add_f32_e32 v8, 1.0, v8
	v_add_f32_e32 v4, 1.0, v10
	v_rcp_f32_e32 v10, v8
	v_add_f32_e32 v8, 1.0, v9
	v_mul_f32_e32 v9, 0xbfb8aa3b, v72
	v_add_f32_e32 v5, 1.0, v11
	v_mul_f32_e32 v6, 0xbfb8aa3b, v68
	v_mul_f32_e32 v7, 0xbfb8aa3b, v69
	v_exp_f32_e32 v9, v9
	v_mul_f32_e32 v11, 0xbfb8aa3b, v73
	v_exp_f32_e32 v6, v6
	v_exp_f32_e32 v7, v7
	v_exp_f32_e32 v11, v11
	v_rcp_f32_e32 v12, v8
	v_add_f32_e32 v8, 1.0, v9
	v_add_f32_e32 v6, 1.0, v6
	v_add_f32_e32 v7, 1.0, v7
	v_rcp_f32_e32 v13, v8
	v_add_f32_e32 v8, 1.0, v11
	v_rcp_f32_e32 v4, v4
	v_rcp_f32_e32 v5, v5
	v_rcp_f32_e32 v6, v6
	v_rcp_f32_e32 v7, v7
	v_rcp_f32_e32 v11, v8
	v_lshl_add_u64 v[8:9], v[2:3], 0, v[56:57]
	v_cvt_pk_bf16_f32 v4, v4, v5
	v_cvt_pk_bf16_f32 v5, v6, v7
	v_cvt_pk_bf16_f32 v6, v10, v12
	v_cvt_pk_bf16_f32 v7, v13, v11
	global_store_dwordx4 v[8:9], v[4:7], off nt
	v_mul_f32_e32 v8, 0xbfb8aa3b, v78
	v_mul_f32_e32 v10, 0xbfb8aa3b, v74
	v_exp_f32_e32 v8, v8
	v_mul_f32_e32 v9, 0xbfb8aa3b, v79
	v_exp_f32_e32 v10, v10
	v_mul_f32_e32 v11, 0xbfb8aa3b, v75
	v_exp_f32_e32 v9, v9
	v_exp_f32_e32 v11, v11
	v_add_f32_e32 v8, 1.0, v8
	v_add_f32_e32 v4, 1.0, v10
	v_rcp_f32_e32 v10, v8
	v_add_f32_e32 v8, 1.0, v9
	v_mul_f32_e32 v9, 0xbfb8aa3b, v80
	v_add_f32_e32 v5, 1.0, v11
	v_mul_f32_e32 v6, 0xbfb8aa3b, v76
	v_mul_f32_e32 v7, 0xbfb8aa3b, v77
	v_exp_f32_e32 v9, v9
	v_mul_f32_e32 v11, 0xbfb8aa3b, v81
	v_exp_f32_e32 v6, v6
	v_exp_f32_e32 v7, v7
	v_exp_f32_e32 v11, v11
	v_rcp_f32_e32 v12, v8
	v_add_f32_e32 v8, 1.0, v9
	v_add_f32_e32 v6, 1.0, v6
	v_add_f32_e32 v7, 1.0, v7
	v_rcp_f32_e32 v13, v8
	v_add_f32_e32 v8, 1.0, v11
	v_rcp_f32_e32 v4, v4
	v_rcp_f32_e32 v5, v5
	v_rcp_f32_e32 v6, v6
	v_rcp_f32_e32 v7, v7
	v_rcp_f32_e32 v11, v8
	v_lshl_add_u64 v[8:9], v[2:3], 0, v[54:55]
	v_cvt_pk_bf16_f32 v4, v4, v5
	v_cvt_pk_bf16_f32 v5, v6, v7
	v_cvt_pk_bf16_f32 v6, v10, v12
	v_cvt_pk_bf16_f32 v7, v13, v11
	global_store_dwordx4 v[8:9], v[4:7], off nt
	v_mul_f32_e32 v8, 0xbfb8aa3b, v86
	v_mul_f32_e32 v10, 0xbfb8aa3b, v82
	v_exp_f32_e32 v8, v8
	v_mul_f32_e32 v9, 0xbfb8aa3b, v87
	v_exp_f32_e32 v10, v10
	v_mul_f32_e32 v11, 0xbfb8aa3b, v83
	v_exp_f32_e32 v9, v9
	v_exp_f32_e32 v11, v11
	v_add_f32_e32 v8, 1.0, v8
	v_add_f32_e32 v4, 1.0, v10
	v_rcp_f32_e32 v10, v8
	v_add_f32_e32 v8, 1.0, v9
	v_mul_f32_e32 v9, 0xbfb8aa3b, v88
	v_add_f32_e32 v5, 1.0, v11
	v_mul_f32_e32 v6, 0xbfb8aa3b, v84
	v_mul_f32_e32 v7, 0xbfb8aa3b, v85
	v_exp_f32_e32 v9, v9
	v_mul_f32_e32 v11, 0xbfb8aa3b, v89
	v_exp_f32_e32 v6, v6
	v_exp_f32_e32 v7, v7
	v_exp_f32_e32 v11, v11
	v_rcp_f32_e32 v12, v8
	v_add_f32_e32 v8, 1.0, v9
	v_add_f32_e32 v6, 1.0, v6
	v_add_f32_e32 v7, 1.0, v7
	v_rcp_f32_e32 v13, v8
	v_add_f32_e32 v8, 1.0, v11
	v_rcp_f32_e32 v4, v4
	v_rcp_f32_e32 v5, v5
	v_rcp_f32_e32 v6, v6
	v_rcp_f32_e32 v7, v7
	v_rcp_f32_e32 v11, v8
	v_lshl_add_u64 v[8:9], v[2:3], 0, v[52:53]
	v_cvt_pk_bf16_f32 v4, v4, v5
	v_cvt_pk_bf16_f32 v5, v6, v7
	v_cvt_pk_bf16_f32 v6, v10, v12
	v_cvt_pk_bf16_f32 v7, v13, v11
	global_store_dwordx4 v[8:9], v[4:7], off nt
	v_mul_f32_e32 v10, 0xbfb8aa3b, v90
	v_exp_f32_e32 v10, v10
	v_mul_f32_e32 v6, 0xbfb8aa3b, v92
	v_exp_f32_e32 v6, v6
	v_mul_f32_e32 v7, 0xbfb8aa3b, v93
	v_exp_f32_e32 v7, v7
	v_mul_f32_e32 v11, 0xbfb8aa3b, v91
	v_add_f32_e32 v6, 1.0, v6
	v_rcp_f32_e32 v8, v6
	v_add_f32_e32 v6, 1.0, v7
	v_mul_f32_e32 v7, 0xbfb8aa3b, v94
	v_exp_f32_e32 v7, v7
	v_mul_f32_e32 v9, 0xbfb8aa3b, v95
	v_exp_f32_e32 v11, v11
	v_exp_f32_e32 v9, v9
	v_add_f32_e32 v4, 1.0, v10
	v_rcp_f32_e32 v10, v6
	v_add_f32_e32 v6, 1.0, v7
	v_mul_f32_e32 v7, 0xbfb8aa3b, v96
	v_add_f32_e32 v5, 1.0, v11
	v_rcp_f32_e32 v11, v6
	v_add_f32_e32 v6, 1.0, v9
	v_exp_f32_e32 v7, v7
	v_mul_f32_e32 v9, 0xbfb8aa3b, v97
	v_exp_f32_e32 v9, v9
	v_rcp_f32_e32 v12, v6
	v_add_f32_e32 v6, 1.0, v7
	v_rcp_f32_e32 v13, v6
	v_add_f32_e32 v6, 1.0, v9
	v_rcp_f32_e32 v4, v4
	v_rcp_f32_e32 v5, v5
	v_rcp_f32_e32 v9, v6
	v_lshl_add_u64 v[6:7], v[2:3], 0, v[50:51]
	v_cvt_pk_bf16_f32 v3, v8, v10
	v_cvt_pk_bf16_f32 v2, v4, v5
	v_cvt_pk_bf16_f32 v4, v11, v12
	v_cvt_pk_bf16_f32 v5, v13, v9
	global_store_dwordx4 v[6:7], v[2:5], off nt

.LBB0_220:
	s_andn2_b64 vcc, exec, s[6:7]
	s_cbranch_vccnz .LBB0_222
	s_add_i32 s31, s29, -10
	s_lshr_b32 s8, s31, 2
	s_lshl_b64 s[6:7], s[8:9], 25
	s_add_u32 s6, s76, s6
	s_addc_u32 s7, s77, s7
	s_lshl_b32 s8, s31, 8
	s_and_b32 s8, s8, 0x200
	v_mov_b32_e32 v2, v235
	v_mov_b32_e32 v3, v240
	s_add_u32 s6, s6, s8
	s_addc_u32 s7, s7, 0
	v_ashrrev_i32_e32 v3, 31, v2
	v_lshl_add_u64 v[6:7], v[2:3], 1, s[6:7]
	v_lshl_add_u64 v[8:9], v[6:7], 0, v[48:49]
	v_cvt_pk_bf16_f32 v2, v106, v107
	v_cvt_pk_bf16_f32 v3, v108, v109
	v_cvt_pk_bf16_f32 v4, v122, v123
	v_cvt_pk_bf16_f32 v5, v124, v125
	global_store_dwordx4 v[8:9], v[2:5], off nt
	v_lshl_add_u64 v[8:9], v[6:7], 0, v[46:47]
	s_nop 0
	v_cvt_pk_bf16_f32 v2, v134, v135
	v_cvt_pk_bf16_f32 v3, v136, v137
	v_cvt_pk_bf16_f32 v4, v146, v147
	v_cvt_pk_bf16_f32 v5, v148, v149
	global_store_dwordx4 v[8:9], v[2:5], off nt
	v_lshl_add_u64 v[8:9], v[6:7], 0, v[44:45]
	s_nop 0
	v_cvt_pk_bf16_f32 v2, v158, v159
	v_cvt_pk_bf16_f32 v3, v160, v161
	v_cvt_pk_bf16_f32 v4, v114, v115
	v_cvt_pk_bf16_f32 v5, v116, v117
	global_store_dwordx4 v[8:9], v[2:5], off nt
	v_lshl_add_u64 v[8:9], v[6:7], 0, v[42:43]
	s_nop 0
	v_cvt_pk_bf16_f32 v2, v126, v127
	v_cvt_pk_bf16_f32 v3, v128, v129
	v_cvt_pk_bf16_f32 v4, v138, v139
	v_cvt_pk_bf16_f32 v5, v140, v141
	global_store_dwordx4 v[8:9], v[2:5], off nt
	v_lshl_add_u64 v[8:9], v[6:7], 0, v[40:41]
	s_nop 0
	v_cvt_pk_bf16_f32 v2, v66, v67
	v_cvt_pk_bf16_f32 v3, v68, v69
	v_cvt_pk_bf16_f32 v4, v70, v71
	v_cvt_pk_bf16_f32 v5, v72, v73
	global_store_dwordx4 v[8:9], v[2:5], off nt
	v_lshl_add_u64 v[8:9], v[6:7], 0, v[38:39]
	s_nop 0
	v_cvt_pk_bf16_f32 v2, v74, v75
	v_cvt_pk_bf16_f32 v3, v76, v77
	v_cvt_pk_bf16_f32 v4, v78, v79
	v_cvt_pk_bf16_f32 v5, v80, v81
	global_store_dwordx4 v[8:9], v[2:5], off nt
	v_lshl_add_u64 v[8:9], v[6:7], 0, v[36:37]
	v_lshl_add_u64 v[6:7], v[6:7], 0, v[34:35]
	v_cvt_pk_bf16_f32 v2, v82, v83
	v_cvt_pk_bf16_f32 v3, v84, v85
	v_cvt_pk_bf16_f32 v4, v86, v87
	v_cvt_pk_bf16_f32 v5, v88, v89
	global_store_dwordx4 v[8:9], v[2:5], off nt
	s_nop 1
	v_cvt_pk_bf16_f32 v2, v90, v91
	v_cvt_pk_bf16_f32 v3, v92, v93
	v_cvt_pk_bf16_f32 v4, v94, v95
	v_cvt_pk_bf16_f32 v5, v96, v97
	global_store_dwordx4 v[6:7], v[2:5], off nt

.LBB0_223:
	s_andn2_b64 vcc, exec, s[6:7]
	s_cbranch_vccnz .LBB0_225
	s_lshl_b32 s8, s42, 8
	s_lshl_b64 s[6:7], s[8:9], 1
	v_mov_b32_e32 v2, v235
	v_mov_b32_e32 v3, v240
	s_add_u32 s6, s76, s6
	s_addc_u32 s7, s77, s7
	v_ashrrev_i32_e32 v3, 31, v2
	v_lshl_add_u64 v[6:7], v[2:3], 1, s[6:7]
	v_pk_mul_f32 v[2:3], v[106:107], s[26:27] op_sel_hi:[1,0]
	v_pk_mul_f32 v[4:5], v[108:109], s[26:27] op_sel_hi:[1,0]
	v_pk_mul_f32 v[8:9], v[122:123], s[26:27] op_sel_hi:[1,0]
	s_waitcnt vmcnt(0)
	v_pk_mul_f32 v[10:11], v[124:125], s[26:27] op_sel_hi:[1,0]
	v_lshl_add_u64 v[12:13], v[6:7], 0, v[48:49]
	v_cvt_pk_bf16_f32 v2, v2, v3
	v_cvt_pk_bf16_f32 v3, v4, v5
	v_cvt_pk_bf16_f32 v4, v8, v9
	v_cvt_pk_bf16_f32 v5, v10, v11
	global_store_dwordx4 v[12:13], v[2:5], off offset:-2560 nt
	v_pk_mul_f32 v[8:9], v[146:147], s[26:27] op_sel_hi:[1,0]
	v_pk_mul_f32 v[10:11], v[148:149], s[26:27] op_sel_hi:[1,0]
	v_pk_mul_f32 v[2:3], v[134:135], s[26:27] op_sel_hi:[1,0]
	v_pk_mul_f32 v[4:5], v[136:137], s[26:27] op_sel_hi:[1,0]
	v_lshl_add_u64 v[12:13], v[6:7], 0, v[46:47]
	v_cvt_pk_bf16_f32 v2, v2, v3
	v_cvt_pk_bf16_f32 v3, v4, v5
	v_cvt_pk_bf16_f32 v4, v8, v9
	v_cvt_pk_bf16_f32 v5, v10, v11
	global_store_dwordx4 v[12:13], v[2:5], off offset:-2560 nt
	v_pk_mul_f32 v[8:9], v[114:115], s[26:27] op_sel_hi:[1,0]
	v_pk_mul_f32 v[10:11], v[116:117], s[26:27] op_sel_hi:[1,0]
	v_pk_mul_f32 v[2:3], v[158:159], s[26:27] op_sel_hi:[1,0]
	v_pk_mul_f32 v[4:5], v[160:161], s[26:27] op_sel_hi:[1,0]
	v_lshl_add_u64 v[12:13], v[6:7], 0, v[44:45]
	v_cvt_pk_bf16_f32 v2, v2, v3
	v_cvt_pk_bf16_f32 v3, v4, v5
	v_cvt_pk_bf16_f32 v4, v8, v9
	v_cvt_pk_bf16_f32 v5, v10, v11
	global_store_dwordx4 v[12:13], v[2:5], off offset:-2560 nt
	v_pk_mul_f32 v[8:9], v[138:139], s[26:27] op_sel_hi:[1,0]
	v_pk_mul_f32 v[10:11], v[140:141], s[26:27] op_sel_hi:[1,0]
	v_pk_mul_f32 v[2:3], v[126:127], s[26:27] op_sel_hi:[1,0]
	v_pk_mul_f32 v[4:5], v[128:129], s[26:27] op_sel_hi:[1,0]
	v_lshl_add_u64 v[12:13], v[6:7], 0, v[42:43]
	v_cvt_pk_bf16_f32 v2, v2, v3
	v_cvt_pk_bf16_f32 v3, v4, v5
	v_cvt_pk_bf16_f32 v4, v8, v9
	v_cvt_pk_bf16_f32 v5, v10, v11
	global_store_dwordx4 v[12:13], v[2:5], off offset:-2560 nt
	v_pk_mul_f32 v[8:9], v[70:71], s[26:27] op_sel_hi:[1,0]
	v_pk_mul_f32 v[10:11], v[72:73], s[26:27] op_sel_hi:[1,0]
	v_pk_mul_f32 v[2:3], v[66:67], s[26:27] op_sel_hi:[1,0]
	v_pk_mul_f32 v[4:5], v[68:69], s[26:27] op_sel_hi:[1,0]
	v_lshl_add_u64 v[12:13], v[6:7], 0, v[40:41]
	v_cvt_pk_bf16_f32 v2, v2, v3
	v_cvt_pk_bf16_f32 v3, v4, v5
	v_cvt_pk_bf16_f32 v4, v8, v9
	v_cvt_pk_bf16_f32 v5, v10, v11
	global_store_dwordx4 v[12:13], v[2:5], off offset:-2560 nt
	v_pk_mul_f32 v[8:9], v[78:79], s[26:27] op_sel_hi:[1,0]
	v_pk_mul_f32 v[10:11], v[80:81], s[26:27] op_sel_hi:[1,0]
	v_pk_mul_f32 v[2:3], v[74:75], s[26:27] op_sel_hi:[1,0]
	v_pk_mul_f32 v[4:5], v[76:77], s[26:27] op_sel_hi:[1,0]
	v_lshl_add_u64 v[12:13], v[6:7], 0, v[38:39]
	v_cvt_pk_bf16_f32 v2, v2, v3
	v_cvt_pk_bf16_f32 v3, v4, v5
	v_cvt_pk_bf16_f32 v4, v8, v9
	v_cvt_pk_bf16_f32 v5, v10, v11
	global_store_dwordx4 v[12:13], v[2:5], off offset:-2560 nt
	v_pk_mul_f32 v[8:9], v[86:87], s[26:27] op_sel_hi:[1,0]
	v_pk_mul_f32 v[10:11], v[88:89], s[26:27] op_sel_hi:[1,0]
	v_pk_mul_f32 v[2:3], v[82:83], s[26:27] op_sel_hi:[1,0]
	v_pk_mul_f32 v[4:5], v[84:85], s[26:27] op_sel_hi:[1,0]
	v_lshl_add_u64 v[12:13], v[6:7], 0, v[36:37]
	v_cvt_pk_bf16_f32 v2, v2, v3
	v_cvt_pk_bf16_f32 v3, v4, v5
	v_cvt_pk_bf16_f32 v4, v8, v9
	v_cvt_pk_bf16_f32 v5, v10, v11
	global_store_dwordx4 v[12:13], v[2:5], off offset:-2560 nt
	v_pk_mul_f32 v[8:9], v[94:95], s[26:27] op_sel_hi:[1,0]
	v_pk_mul_f32 v[10:11], v[96:97], s[26:27] op_sel_hi:[1,0]
	v_pk_mul_f32 v[2:3], v[90:91], s[26:27] op_sel_hi:[1,0]
	v_pk_mul_f32 v[4:5], v[92:93], s[26:27] op_sel_hi:[1,0]
	v_lshl_add_u64 v[6:7], v[6:7], 0, v[34:35]
	v_cvt_pk_bf16_f32 v2, v2, v3
	v_cvt_pk_bf16_f32 v3, v4, v5
	v_cvt_pk_bf16_f32 v4, v8, v9
	v_cvt_pk_bf16_f32 v5, v10, v11
	global_store_dwordx4 v[6:7], v[2:5], off offset:-2560 nt

.LBB0_226:
	s_andn2_b64 vcc, exec, s[6:7]
	s_cbranch_vccnz .LBB0_228
	v_mov_b32_e32 v2, v235
	v_mov_b32_e32 v3, v240
	s_add_u32 s6, s74, s44
	s_addc_u32 s7, s75, s45
	v_ashrrev_i32_e32 v3, 31, v2
	v_lshl_add_u64 v[6:7], v[2:3], 1, s[6:7]
	v_lshl_add_u64 v[8:9], v[6:7], 0, v[32:33]
	v_cvt_pk_bf16_f32 v2, v106, v107
	v_cvt_pk_bf16_f32 v3, v108, v109
	v_cvt_pk_bf16_f32 v4, v122, v123
	v_cvt_pk_bf16_f32 v5, v124, v125
	global_store_dwordx4 v[8:9], v[2:5], off nt
	v_lshl_add_u64 v[8:9], v[6:7], 0, v[30:31]
	s_nop 0
	v_cvt_pk_bf16_f32 v2, v134, v135
	v_cvt_pk_bf16_f32 v3, v136, v137
	v_cvt_pk_bf16_f32 v4, v146, v147
	v_cvt_pk_bf16_f32 v5, v148, v149
	global_store_dwordx4 v[8:9], v[2:5], off nt
	v_lshl_add_u64 v[8:9], v[6:7], 0, v[28:29]
	s_nop 0
	v_cvt_pk_bf16_f32 v2, v158, v159
	v_cvt_pk_bf16_f32 v3, v160, v161
	v_cvt_pk_bf16_f32 v4, v114, v115
	v_cvt_pk_bf16_f32 v5, v116, v117
	global_store_dwordx4 v[8:9], v[2:5], off nt
	v_lshl_add_u64 v[8:9], v[6:7], 0, v[26:27]
	s_nop 0
	v_cvt_pk_bf16_f32 v2, v126, v127
	v_cvt_pk_bf16_f32 v3, v128, v129
	v_cvt_pk_bf16_f32 v4, v138, v139
	v_cvt_pk_bf16_f32 v5, v140, v141
	global_store_dwordx4 v[8:9], v[2:5], off nt
	v_lshl_add_u64 v[8:9], v[6:7], 0, v[24:25]
	s_nop 0
	v_cvt_pk_bf16_f32 v2, v66, v67
	v_cvt_pk_bf16_f32 v3, v68, v69
	v_cvt_pk_bf16_f32 v4, v70, v71
	v_cvt_pk_bf16_f32 v5, v72, v73
	global_store_dwordx4 v[8:9], v[2:5], off nt
	v_lshl_add_u64 v[8:9], v[6:7], 0, v[22:23]
	s_nop 0
	v_cvt_pk_bf16_f32 v2, v74, v75
	v_cvt_pk_bf16_f32 v3, v76, v77
	v_cvt_pk_bf16_f32 v4, v78, v79
	v_cvt_pk_bf16_f32 v5, v80, v81
	global_store_dwordx4 v[8:9], v[2:5], off nt
	v_lshl_add_u64 v[8:9], v[6:7], 0, v[20:21]
	v_lshl_add_u64 v[6:7], v[6:7], 0, v[18:19]
	v_cvt_pk_bf16_f32 v2, v82, v83
	v_cvt_pk_bf16_f32 v3, v84, v85
	v_cvt_pk_bf16_f32 v4, v86, v87
	v_cvt_pk_bf16_f32 v5, v88, v89
	global_store_dwordx4 v[8:9], v[2:5], off nt
	s_nop 1
	v_cvt_pk_bf16_f32 v2, v90, v91
	v_cvt_pk_bf16_f32 v3, v92, v93
	v_cvt_pk_bf16_f32 v4, v94, v95
	v_cvt_pk_bf16_f32 v5, v96, v97
	global_store_dwordx4 v[6:7], v[2:5], off nt

.LBB0_233:
	s_waitcnt vmcnt(0)
	v_add_u32_e32 v10, 0x400, v224
	global_load_dwordx4 v[6:9], v10, s[14:15] offset:48
	global_load_dwordx4 v[14:17], v10, s[14:15] offset:32
	global_load_dwordx4 v[2:5], v10, s[14:15] offset:16
	s_nop 0
	global_load_dwordx4 v[10:13], v10, s[14:15]
	s_add_u32 s44, s74, s44
	s_addc_u32 s45, s75, s45
	v_ashrrev_i32_e32 v223, 31, v222
	v_lshl_add_u64 v[222:223], v[222:223], 1, s[44:45]
	v_lshl_add_u64 v[242:243], v[222:223], 0, v[32:33]
	v_cvt_pk_bf16_f32 v226, v225, v226
	v_cvt_pk_bf16_f32 v227, v227, v228
	v_cvt_pk_bf16_f32 v228, v229, v230
	v_cvt_pk_bf16_f32 v229, v231, v232
	s_and_b64 vcc, exec, s[6:7]
	global_store_dwordx4 v[242:243], v[226:229], off nt
	s_cbranch_vccnz .LBB0_235
	s_nop 0
	v_and_b32_e32 v226, 64, v239
	v_xor_b32_e32 v225, 16, v239
	v_add_u32_e32 v226, 64, v226
	v_cmp_lt_i32_e32 vcc, v225, v226
	s_nop 1
	v_cndmask_b32_e32 v225, v239, v225, vcc
	v_lshlrev_b32_e32 v231, 2, v225
	ds_bpermute_b32 v225, v231, v134
	ds_bpermute_b32 v226, v231, v135
	s_waitcnt vmcnt(3) lgkmcnt(1)
	v_mul_f32_e32 v14, v14, v225
	v_cndmask_b32_e64 v14, v14, -v14, s[0:1]
	s_waitcnt vmcnt(1)
	v_fmac_f32_e32 v14, v134, v10
	ds_bpermute_b32 v10, v231, v136
	s_waitcnt lgkmcnt(1)
	v_mul_f32_e32 v15, v15, v226
	v_cndmask_b32_e64 v225, v134, v14, s[2:3]
	v_cndmask_b32_e64 v14, v15, -v15, s[0:1]
	v_fmac_f32_e32 v14, v135, v11
	ds_bpermute_b32 v11, v231, v137
	s_waitcnt lgkmcnt(1)
	v_mul_f32_e32 v10, v16, v10
	v_cndmask_b32_e64 v10, v10, -v10, s[0:1]
	v_fmac_f32_e32 v10, v136, v12
	v_cndmask_b32_e64 v227, v136, v10, s[2:3]
	s_waitcnt lgkmcnt(0)
	v_mul_f32_e32 v10, v17, v11
	ds_bpermute_b32 v11, v231, v146
	v_cndmask_b32_e64 v10, v10, -v10, s[0:1]
	v_fmac_f32_e32 v10, v137, v13
	v_cndmask_b32_e64 v228, v137, v10, s[2:3]
	ds_bpermute_b32 v10, v231, v147
	s_waitcnt lgkmcnt(1)
	v_mul_f32_e32 v6, v6, v11
	v_cndmask_b32_e64 v6, v6, -v6, s[0:1]
	v_fmac_f32_e32 v6, v146, v2
	v_cndmask_b32_e64 v229, v146, v6, s[2:3]
	s_waitcnt lgkmcnt(0)
	v_mul_f32_e32 v2, v7, v10
	v_cndmask_b32_e64 v2, v2, -v2, s[0:1]
	v_fmac_f32_e32 v2, v147, v3
	ds_bpermute_b32 v6, v231, v148
	v_cndmask_b32_e64 v230, v147, v2, s[2:3]
	ds_bpermute_b32 v2, v231, v149
	v_cndmask_b32_e64 v226, v135, v14, s[2:3]
	s_waitcnt lgkmcnt(1)
	v_mul_f32_e32 v3, v8, v6
	v_cndmask_b32_e64 v3, v3, -v3, s[0:1]
	s_waitcnt lgkmcnt(0)
	v_mul_f32_e32 v2, v9, v2
	v_cndmask_b32_e64 v2, v2, -v2, s[0:1]
	v_fmac_f32_e32 v3, v148, v4
	v_fmac_f32_e32 v2, v149, v5
	v_cndmask_b32_e64 v231, v148, v3, s[2:3]
	v_cndmask_b32_e64 v232, v149, v2, s[2:3]
	s_branch .LBB0_236

.LBB0_236:
	s_waitcnt vmcnt(1)
	v_add_u32_e32 v10, 0x800, v224
	global_load_dwordx4 v[6:9], v10, s[14:15] offset:48
	global_load_dwordx4 v[14:17], v10, s[14:15] offset:32
	global_load_dwordx4 v[2:5], v10, s[14:15] offset:16
	s_nop 0
	global_load_dwordx4 v[10:13], v10, s[14:15]
	v_lshl_add_u64 v[242:243], v[222:223], 0, v[30:31]
	v_cvt_pk_bf16_f32 v226, v225, v226
	v_cvt_pk_bf16_f32 v227, v227, v228
	v_cvt_pk_bf16_f32 v228, v229, v230
	v_cvt_pk_bf16_f32 v229, v231, v232
	s_and_b64 vcc, exec, s[6:7]
	global_store_dwordx4 v[242:243], v[226:229], off nt
	s_cbranch_vccnz .LBB0_238
	s_nop 0
	v_and_b32_e32 v226, 64, v239
	v_xor_b32_e32 v225, 16, v239
	v_add_u32_e32 v226, 64, v226
	v_cmp_lt_i32_e32 vcc, v225, v226
	s_nop 1
	v_cndmask_b32_e32 v225, v239, v225, vcc
	v_lshlrev_b32_e32 v231, 2, v225
	ds_bpermute_b32 v225, v231, v158
	ds_bpermute_b32 v226, v231, v159
	s_waitcnt vmcnt(3) lgkmcnt(1)
	v_mul_f32_e32 v14, v14, v225
	v_cndmask_b32_e64 v14, v14, -v14, s[0:1]
	s_waitcnt vmcnt(1)
	v_fmac_f32_e32 v14, v158, v10
	ds_bpermute_b32 v10, v231, v160
	s_waitcnt lgkmcnt(1)
	v_mul_f32_e32 v15, v15, v226
	v_cndmask_b32_e64 v225, v158, v14, s[2:3]
	v_cndmask_b32_e64 v14, v15, -v15, s[0:1]
	v_fmac_f32_e32 v14, v159, v11
	ds_bpermute_b32 v11, v231, v161
	s_waitcnt lgkmcnt(1)
	v_mul_f32_e32 v10, v16, v10
	v_cndmask_b32_e64 v10, v10, -v10, s[0:1]
	v_fmac_f32_e32 v10, v160, v12
	v_cndmask_b32_e64 v227, v160, v10, s[2:3]
	s_waitcnt lgkmcnt(0)
	v_mul_f32_e32 v10, v17, v11
	ds_bpermute_b32 v11, v231, v114
	v_cndmask_b32_e64 v10, v10, -v10, s[0:1]
	v_fmac_f32_e32 v10, v161, v13
	v_cndmask_b32_e64 v228, v161, v10, s[2:3]
	ds_bpermute_b32 v10, v231, v115
	s_waitcnt lgkmcnt(1)
	v_mul_f32_e32 v6, v6, v11
	v_cndmask_b32_e64 v6, v6, -v6, s[0:1]
	v_fmac_f32_e32 v6, v114, v2
	v_cndmask_b32_e64 v229, v114, v6, s[2:3]
	s_waitcnt lgkmcnt(0)
	v_mul_f32_e32 v2, v7, v10
	v_cndmask_b32_e64 v2, v2, -v2, s[0:1]
	v_fmac_f32_e32 v2, v115, v3
	ds_bpermute_b32 v6, v231, v116
	v_cndmask_b32_e64 v230, v115, v2, s[2:3]
	ds_bpermute_b32 v2, v231, v117
	v_cndmask_b32_e64 v226, v159, v14, s[2:3]
	s_waitcnt lgkmcnt(1)
	v_mul_f32_e32 v3, v8, v6
	v_cndmask_b32_e64 v3, v3, -v3, s[0:1]
	s_waitcnt lgkmcnt(0)
	v_mul_f32_e32 v2, v9, v2
	v_cndmask_b32_e64 v2, v2, -v2, s[0:1]
	v_fmac_f32_e32 v3, v116, v4
	v_fmac_f32_e32 v2, v117, v5
	v_cndmask_b32_e64 v231, v116, v3, s[2:3]
	v_cndmask_b32_e64 v232, v117, v2, s[2:3]
	s_branch .LBB0_239

.LBB0_239:
	s_waitcnt vmcnt(1)
	v_add_u32_e32 v10, 0xc00, v224
	global_load_dwordx4 v[6:9], v10, s[14:15] offset:48
	global_load_dwordx4 v[14:17], v10, s[14:15] offset:32
	global_load_dwordx4 v[2:5], v10, s[14:15] offset:16
	s_nop 0
	global_load_dwordx4 v[10:13], v10, s[14:15]
	v_lshl_add_u64 v[242:243], v[222:223], 0, v[28:29]
	v_cvt_pk_bf16_f32 v226, v225, v226
	v_cvt_pk_bf16_f32 v227, v227, v228
	v_cvt_pk_bf16_f32 v228, v229, v230
	v_cvt_pk_bf16_f32 v229, v231, v232
	s_and_b64 vcc, exec, s[6:7]
	global_store_dwordx4 v[242:243], v[226:229], off nt
	s_cbranch_vccnz .LBB0_241
	s_nop 0
	v_and_b32_e32 v226, 64, v239
	v_xor_b32_e32 v225, 16, v239
	v_add_u32_e32 v226, 64, v226
	v_cmp_lt_i32_e32 vcc, v225, v226
	s_nop 1
	v_cndmask_b32_e32 v225, v239, v225, vcc
	v_lshlrev_b32_e32 v231, 2, v225
	ds_bpermute_b32 v225, v231, v126
	ds_bpermute_b32 v226, v231, v127
	s_waitcnt vmcnt(3) lgkmcnt(1)
	v_mul_f32_e32 v14, v14, v225
	v_cndmask_b32_e64 v14, v14, -v14, s[0:1]
	s_waitcnt vmcnt(1)
	v_fmac_f32_e32 v14, v126, v10
	ds_bpermute_b32 v10, v231, v128
	s_waitcnt lgkmcnt(1)
	v_mul_f32_e32 v15, v15, v226
	v_cndmask_b32_e64 v225, v126, v14, s[2:3]
	v_cndmask_b32_e64 v14, v15, -v15, s[0:1]
	v_fmac_f32_e32 v14, v127, v11
	ds_bpermute_b32 v11, v231, v129
	s_waitcnt lgkmcnt(1)
	v_mul_f32_e32 v10, v16, v10
	v_cndmask_b32_e64 v10, v10, -v10, s[0:1]
	v_fmac_f32_e32 v10, v128, v12
	v_cndmask_b32_e64 v227, v128, v10, s[2:3]
	s_waitcnt lgkmcnt(0)
	v_mul_f32_e32 v10, v17, v11
	ds_bpermute_b32 v11, v231, v138
	v_cndmask_b32_e64 v10, v10, -v10, s[0:1]
	v_fmac_f32_e32 v10, v129, v13
	v_cndmask_b32_e64 v228, v129, v10, s[2:3]
	ds_bpermute_b32 v10, v231, v139
	s_waitcnt lgkmcnt(1)
	v_mul_f32_e32 v6, v6, v11
	v_cndmask_b32_e64 v6, v6, -v6, s[0:1]
	v_fmac_f32_e32 v6, v138, v2
	v_cndmask_b32_e64 v229, v138, v6, s[2:3]
	s_waitcnt lgkmcnt(0)
	v_mul_f32_e32 v2, v7, v10
	v_cndmask_b32_e64 v2, v2, -v2, s[0:1]
	v_fmac_f32_e32 v2, v139, v3
	ds_bpermute_b32 v6, v231, v140
	v_cndmask_b32_e64 v230, v139, v2, s[2:3]
	ds_bpermute_b32 v2, v231, v141
	v_cndmask_b32_e64 v226, v127, v14, s[2:3]
	s_waitcnt lgkmcnt(1)
	v_mul_f32_e32 v3, v8, v6
	v_cndmask_b32_e64 v3, v3, -v3, s[0:1]
	s_waitcnt lgkmcnt(0)
	v_mul_f32_e32 v2, v9, v2
	v_cndmask_b32_e64 v2, v2, -v2, s[0:1]
	v_fmac_f32_e32 v3, v140, v4
	v_fmac_f32_e32 v2, v141, v5
	v_cndmask_b32_e64 v231, v140, v3, s[2:3]
	v_cndmask_b32_e64 v232, v141, v2, s[2:3]
	s_branch .LBB0_242

.LBB0_242:
	s_waitcnt vmcnt(1)
	v_add_u32_e32 v10, 0x2000, v224
	global_load_dwordx4 v[6:9], v10, s[14:15] offset:48
	global_load_dwordx4 v[14:17], v10, s[14:15] offset:32
	global_load_dwordx4 v[2:5], v10, s[14:15] offset:16
	s_nop 0
	global_load_dwordx4 v[10:13], v10, s[14:15]
	v_lshl_add_u64 v[242:243], v[222:223], 0, v[26:27]
	v_cvt_pk_bf16_f32 v226, v225, v226
	v_cvt_pk_bf16_f32 v227, v227, v228
	v_cvt_pk_bf16_f32 v228, v229, v230
	v_cvt_pk_bf16_f32 v229, v231, v232
	s_and_b64 vcc, exec, s[6:7]
	global_store_dwordx4 v[242:243], v[226:229], off nt
	s_cbranch_vccnz .LBB0_244
	s_nop 0
	v_and_b32_e32 v226, 64, v239
	v_xor_b32_e32 v225, 16, v239
	v_add_u32_e32 v226, 64, v226
	v_cmp_lt_i32_e32 vcc, v225, v226
	s_nop 1
	v_cndmask_b32_e32 v225, v239, v225, vcc
	v_lshlrev_b32_e32 v231, 2, v225
	ds_bpermute_b32 v225, v231, v66
	ds_bpermute_b32 v226, v231, v67
	s_waitcnt vmcnt(3) lgkmcnt(1)
	v_mul_f32_e32 v14, v14, v225
	v_cndmask_b32_e64 v14, v14, -v14, s[0:1]
	s_waitcnt vmcnt(1)
	v_fmac_f32_e32 v14, v66, v10
	ds_bpermute_b32 v10, v231, v68
	s_waitcnt lgkmcnt(1)
	v_mul_f32_e32 v15, v15, v226
	v_cndmask_b32_e64 v225, v66, v14, s[2:3]
	v_cndmask_b32_e64 v14, v15, -v15, s[0:1]
	v_fmac_f32_e32 v14, v67, v11
	ds_bpermute_b32 v11, v231, v69
	s_waitcnt lgkmcnt(1)
	v_mul_f32_e32 v10, v16, v10
	v_cndmask_b32_e64 v10, v10, -v10, s[0:1]
	v_fmac_f32_e32 v10, v68, v12
	v_cndmask_b32_e64 v227, v68, v10, s[2:3]
	s_waitcnt lgkmcnt(0)
	v_mul_f32_e32 v10, v17, v11
	ds_bpermute_b32 v11, v231, v70
	v_cndmask_b32_e64 v10, v10, -v10, s[0:1]
	v_fmac_f32_e32 v10, v69, v13
	v_cndmask_b32_e64 v228, v69, v10, s[2:3]
	ds_bpermute_b32 v10, v231, v71
	s_waitcnt lgkmcnt(1)
	v_mul_f32_e32 v6, v6, v11
	v_cndmask_b32_e64 v6, v6, -v6, s[0:1]
	v_fmac_f32_e32 v6, v70, v2
	v_cndmask_b32_e64 v229, v70, v6, s[2:3]
	s_waitcnt lgkmcnt(0)
	v_mul_f32_e32 v2, v7, v10
	v_cndmask_b32_e64 v2, v2, -v2, s[0:1]
	v_fmac_f32_e32 v2, v71, v3
	ds_bpermute_b32 v6, v231, v72
	v_cndmask_b32_e64 v230, v71, v2, s[2:3]
	ds_bpermute_b32 v2, v231, v73
	v_cndmask_b32_e64 v226, v67, v14, s[2:3]
	s_waitcnt lgkmcnt(1)
	v_mul_f32_e32 v3, v8, v6
	v_cndmask_b32_e64 v3, v3, -v3, s[0:1]
	s_waitcnt lgkmcnt(0)
	v_mul_f32_e32 v2, v9, v2
	v_cndmask_b32_e64 v2, v2, -v2, s[0:1]
	v_fmac_f32_e32 v3, v72, v4
	v_fmac_f32_e32 v2, v73, v5
	v_cndmask_b32_e64 v231, v72, v3, s[2:3]
	v_cndmask_b32_e64 v232, v73, v2, s[2:3]
	s_branch .LBB0_245

.LBB0_245:
	s_waitcnt vmcnt(1)
	v_add_u32_e32 v10, 0x2400, v224
	global_load_dwordx4 v[6:9], v10, s[14:15] offset:48
	global_load_dwordx4 v[14:17], v10, s[14:15] offset:32
	global_load_dwordx4 v[2:5], v10, s[14:15] offset:16
	s_nop 0
	global_load_dwordx4 v[10:13], v10, s[14:15]
	v_lshl_add_u64 v[242:243], v[222:223], 0, v[24:25]
	v_cvt_pk_bf16_f32 v226, v225, v226
	v_cvt_pk_bf16_f32 v227, v227, v228
	v_cvt_pk_bf16_f32 v228, v229, v230
	v_cvt_pk_bf16_f32 v229, v231, v232
	s_and_b64 vcc, exec, s[6:7]
	global_store_dwordx4 v[242:243], v[226:229], off nt
	s_cbranch_vccnz .LBB0_247
	s_nop 0
	v_and_b32_e32 v226, 64, v239
	v_xor_b32_e32 v225, 16, v239
	v_add_u32_e32 v226, 64, v226
	v_cmp_lt_i32_e32 vcc, v225, v226
	s_nop 1
	v_cndmask_b32_e32 v225, v239, v225, vcc
	v_lshlrev_b32_e32 v231, 2, v225
	ds_bpermute_b32 v225, v231, v74
	ds_bpermute_b32 v226, v231, v75
	s_waitcnt vmcnt(3) lgkmcnt(1)
	v_mul_f32_e32 v14, v14, v225
	v_cndmask_b32_e64 v14, v14, -v14, s[0:1]
	s_waitcnt vmcnt(1)
	v_fmac_f32_e32 v14, v74, v10
	ds_bpermute_b32 v10, v231, v76
	s_waitcnt lgkmcnt(1)
	v_mul_f32_e32 v15, v15, v226
	v_cndmask_b32_e64 v225, v74, v14, s[2:3]
	v_cndmask_b32_e64 v14, v15, -v15, s[0:1]
	v_fmac_f32_e32 v14, v75, v11
	ds_bpermute_b32 v11, v231, v77
	s_waitcnt lgkmcnt(1)
	v_mul_f32_e32 v10, v16, v10
	v_cndmask_b32_e64 v10, v10, -v10, s[0:1]
	v_fmac_f32_e32 v10, v76, v12
	v_cndmask_b32_e64 v227, v76, v10, s[2:3]
	s_waitcnt lgkmcnt(0)
	v_mul_f32_e32 v10, v17, v11
	ds_bpermute_b32 v11, v231, v78
	v_cndmask_b32_e64 v10, v10, -v10, s[0:1]
	v_fmac_f32_e32 v10, v77, v13
	v_cndmask_b32_e64 v228, v77, v10, s[2:3]
	ds_bpermute_b32 v10, v231, v79
	s_waitcnt lgkmcnt(1)
	v_mul_f32_e32 v6, v6, v11
	v_cndmask_b32_e64 v6, v6, -v6, s[0:1]
	v_fmac_f32_e32 v6, v78, v2
	v_cndmask_b32_e64 v229, v78, v6, s[2:3]
	s_waitcnt lgkmcnt(0)
	v_mul_f32_e32 v2, v7, v10
	v_cndmask_b32_e64 v2, v2, -v2, s[0:1]
	v_fmac_f32_e32 v2, v79, v3
	ds_bpermute_b32 v6, v231, v80
	v_cndmask_b32_e64 v230, v79, v2, s[2:3]
	ds_bpermute_b32 v2, v231, v81
	v_cndmask_b32_e64 v226, v75, v14, s[2:3]
	s_waitcnt lgkmcnt(1)
	v_mul_f32_e32 v3, v8, v6
	v_cndmask_b32_e64 v3, v3, -v3, s[0:1]
	s_waitcnt lgkmcnt(0)
	v_mul_f32_e32 v2, v9, v2
	v_cndmask_b32_e64 v2, v2, -v2, s[0:1]
	v_fmac_f32_e32 v3, v80, v4
	v_fmac_f32_e32 v2, v81, v5
	v_cndmask_b32_e64 v231, v80, v3, s[2:3]
	v_cndmask_b32_e64 v232, v81, v2, s[2:3]
	s_branch .LBB0_248

.LBB0_248:
	s_waitcnt vmcnt(1)
	v_add_u32_e32 v10, 0x2800, v224
	global_load_dwordx4 v[6:9], v10, s[14:15] offset:48
	global_load_dwordx4 v[14:17], v10, s[14:15] offset:32
	global_load_dwordx4 v[2:5], v10, s[14:15] offset:16
	s_nop 0
	global_load_dwordx4 v[10:13], v10, s[14:15]
	v_lshl_add_u64 v[242:243], v[222:223], 0, v[22:23]
	v_cvt_pk_bf16_f32 v226, v225, v226
	v_cvt_pk_bf16_f32 v227, v227, v228
	v_cvt_pk_bf16_f32 v228, v229, v230
	v_cvt_pk_bf16_f32 v229, v231, v232
	s_and_b64 vcc, exec, s[6:7]
	global_store_dwordx4 v[242:243], v[226:229], off nt
	s_cbranch_vccnz .LBB0_250
	s_nop 0
	v_and_b32_e32 v226, 64, v239
	v_xor_b32_e32 v225, 16, v239
	v_add_u32_e32 v226, 64, v226
	v_cmp_lt_i32_e32 vcc, v225, v226
	s_nop 1
	v_cndmask_b32_e32 v225, v239, v225, vcc
	v_lshlrev_b32_e32 v231, 2, v225
	ds_bpermute_b32 v225, v231, v82
	ds_bpermute_b32 v226, v231, v83
	s_waitcnt vmcnt(3) lgkmcnt(1)
	v_mul_f32_e32 v14, v14, v225
	v_cndmask_b32_e64 v14, v14, -v14, s[0:1]
	s_waitcnt vmcnt(1)
	v_fmac_f32_e32 v14, v82, v10
	ds_bpermute_b32 v10, v231, v84
	s_waitcnt lgkmcnt(1)
	v_mul_f32_e32 v15, v15, v226
	v_cndmask_b32_e64 v225, v82, v14, s[2:3]
	v_cndmask_b32_e64 v14, v15, -v15, s[0:1]
	v_fmac_f32_e32 v14, v83, v11
	ds_bpermute_b32 v11, v231, v85
	s_waitcnt lgkmcnt(1)
	v_mul_f32_e32 v10, v16, v10
	v_cndmask_b32_e64 v10, v10, -v10, s[0:1]
	v_fmac_f32_e32 v10, v84, v12
	v_cndmask_b32_e64 v227, v84, v10, s[2:3]
	s_waitcnt lgkmcnt(0)
	v_mul_f32_e32 v10, v17, v11
	ds_bpermute_b32 v11, v231, v86
	v_cndmask_b32_e64 v10, v10, -v10, s[0:1]
	v_fmac_f32_e32 v10, v85, v13
	v_cndmask_b32_e64 v228, v85, v10, s[2:3]
	ds_bpermute_b32 v10, v231, v87
	s_waitcnt lgkmcnt(1)
	v_mul_f32_e32 v6, v6, v11
	v_cndmask_b32_e64 v6, v6, -v6, s[0:1]
	v_fmac_f32_e32 v6, v86, v2
	v_cndmask_b32_e64 v229, v86, v6, s[2:3]
	s_waitcnt lgkmcnt(0)
	v_mul_f32_e32 v2, v7, v10
	v_cndmask_b32_e64 v2, v2, -v2, s[0:1]
	v_fmac_f32_e32 v2, v87, v3
	ds_bpermute_b32 v6, v231, v88
	v_cndmask_b32_e64 v230, v87, v2, s[2:3]
	ds_bpermute_b32 v2, v231, v89
	v_cndmask_b32_e64 v226, v83, v14, s[2:3]
	s_waitcnt lgkmcnt(1)
	v_mul_f32_e32 v3, v8, v6
	v_cndmask_b32_e64 v3, v3, -v3, s[0:1]
	s_waitcnt lgkmcnt(0)
	v_mul_f32_e32 v2, v9, v2
	v_cndmask_b32_e64 v2, v2, -v2, s[0:1]
	v_fmac_f32_e32 v3, v88, v4
	v_fmac_f32_e32 v2, v89, v5
	v_cndmask_b32_e64 v231, v88, v3, s[2:3]
	v_cndmask_b32_e64 v232, v89, v2, s[2:3]
	s_branch .LBB0_251

.LBB0_251:
	s_waitcnt vmcnt(1)
	v_add_u32_e32 v10, 0x2c00, v224
	global_load_dwordx4 v[6:9], v10, s[14:15] offset:48
	global_load_dwordx4 v[14:17], v10, s[14:15] offset:32
	global_load_dwordx4 v[2:5], v10, s[14:15] offset:16
	s_nop 0
	global_load_dwordx4 v[10:13], v10, s[14:15]
	v_lshl_add_u64 v[242:243], v[222:223], 0, v[20:21]
	v_cvt_pk_bf16_f32 v224, v225, v226
	v_cvt_pk_bf16_f32 v225, v227, v228
	v_cvt_pk_bf16_f32 v226, v229, v230
	v_cvt_pk_bf16_f32 v227, v231, v232
	s_and_b64 vcc, exec, s[6:7]
	global_store_dwordx4 v[242:243], v[224:227], off nt
	s_cbranch_vccnz .LBB0_253
	s_nop 0
	v_and_b32_e32 v225, 64, v239
	v_xor_b32_e32 v224, 16, v239
	v_add_u32_e32 v225, 64, v225
	v_cmp_lt_i32_e32 vcc, v224, v225
	s_nop 1
	v_cndmask_b32_e32 v224, v239, v224, vcc
	v_lshlrev_b32_e32 v224, 2, v224
	ds_bpermute_b32 v225, v224, v90
	ds_bpermute_b32 v226, v224, v91
	s_waitcnt vmcnt(3) lgkmcnt(1)
	v_mul_f32_e32 v14, v14, v225
	v_cndmask_b32_e64 v14, v14, -v14, s[0:1]
	s_waitcnt vmcnt(1)
	v_fmac_f32_e32 v14, v90, v10
	s_waitcnt lgkmcnt(0)
	v_mul_f32_e32 v15, v15, v226
	v_cndmask_b32_e64 v10, v90, v14, s[2:3]
	ds_bpermute_b32 v14, v224, v92
	v_cndmask_b32_e64 v15, v15, -v15, s[0:1]
	v_fmac_f32_e32 v15, v91, v11
	v_cndmask_b32_e64 v11, v91, v15, s[2:3]
	ds_bpermute_b32 v15, v224, v93
	s_waitcnt lgkmcnt(1)
	v_mul_f32_e32 v14, v16, v14
	v_cndmask_b32_e64 v14, v14, -v14, s[0:1]
	v_fmac_f32_e32 v14, v92, v12
	v_cndmask_b32_e64 v12, v92, v14, s[2:3]
	s_waitcnt lgkmcnt(0)
	v_mul_f32_e32 v14, v17, v15
	ds_bpermute_b32 v15, v224, v94
	v_cndmask_b32_e64 v14, v14, -v14, s[0:1]
	v_fmac_f32_e32 v14, v93, v13
	v_cndmask_b32_e64 v13, v93, v14, s[2:3]
	ds_bpermute_b32 v14, v224, v95
	s_waitcnt lgkmcnt(1)
	v_mul_f32_e32 v6, v6, v15
	v_cndmask_b32_e64 v6, v6, -v6, s[0:1]
	v_fmac_f32_e32 v6, v94, v2
	v_cndmask_b32_e64 v2, v94, v6, s[2:3]
	s_waitcnt lgkmcnt(0)
	v_mul_f32_e32 v6, v7, v14
	v_cndmask_b32_e64 v6, v6, -v6, s[0:1]
	v_fmac_f32_e32 v6, v95, v3
	ds_bpermute_b32 v7, v224, v96
	v_cndmask_b32_e64 v3, v95, v6, s[2:3]
	ds_bpermute_b32 v6, v224, v97
	s_waitcnt lgkmcnt(1)
	v_mul_f32_e32 v7, v8, v7
	v_cndmask_b32_e64 v7, v7, -v7, s[0:1]
	s_waitcnt lgkmcnt(0)
	v_mul_f32_e32 v6, v9, v6
	v_cndmask_b32_e64 v6, v6, -v6, s[0:1]
	v_fmac_f32_e32 v7, v96, v4
	v_fmac_f32_e32 v6, v97, v5
	v_cndmask_b32_e64 v4, v96, v7, s[2:3]
	v_cndmask_b32_e64 v5, v97, v6, s[2:3]
	s_branch .LBB0_254

.LBB0_254:
	v_lshl_add_u64 v[14:15], v[222:223], 0, v[18:19]
	v_cvt_pk_bf16_f32 v6, v10, v11
	v_cvt_pk_bf16_f32 v7, v12, v13
	v_cvt_pk_bf16_f32 v8, v2, v3
	v_cvt_pk_bf16_f32 v9, v4, v5
	global_store_dwordx4 v[14:15], v[6:9], off nt

.LBB0_263:
	s_waitcnt vmcnt(0)
	v_add_u32_e32 v10, 0x400, v241
	global_load_dwordx4 v[6:9], v10, s[14:15] offset:48
	global_load_dwordx4 v[14:17], v10, s[14:15] offset:32
	global_load_dwordx4 v[2:5], v10, s[14:15] offset:16
	s_nop 0
	global_load_dwordx4 v[10:13], v10, s[14:15]
	s_lshl_b32 s42, s42, 8
	s_ashr_i32 s43, s42, 31
	s_lshl_b64 s[42:43], s[42:43], 1
	s_add_u32 s44, s70, s42
	s_addc_u32 s45, s71, s43
	v_ashrrev_i32_e32 v215, 31, v214
	s_add_u32 s42, s72, s42
	v_lshlrev_b64 v[214:215], 1, v[214:215]
	s_addc_u32 s43, s73, s43
	v_lshl_add_u64 v[216:217], s[44:45], 0, v[214:215]
	v_lshlrev_b64 v[250:251], 1, v[228:229]
	v_lshl_add_u64 v[214:215], s[42:43], 0, v[214:215]
	v_lshl_add_u64 v[252:253], v[216:217], 0, v[250:251]
	v_cvt_pk_bf16_f32 v218, v218, v219
	v_cvt_pk_bf16_f32 v219, v220, v221
	v_cvt_pk_bf16_f32 v220, v230, v231
	v_cvt_pk_bf16_f32 v221, v232, v233
	global_store_dwordx4 v[252:253], v[218:221], off nt
	v_lshl_add_u64 v[230:231], v[214:215], 0, v[250:251]
	s_and_b64 vcc, exec, s[6:7]
	v_cvt_pk_bf16_f32 v218, v242, v243
	v_cvt_pk_bf16_f32 v219, v244, v245
	v_cvt_pk_bf16_f32 v220, v246, v247
	v_cvt_pk_bf16_f32 v221, v248, v249
	global_store_dwordx4 v[230:231], v[218:221], off nt
	v_pk_mul_f32 v[230:231], v[146:147], s[26:27] op_sel_hi:[1,0]
	v_pk_mul_f32 v[232:233], v[148:149], s[26:27] op_sel_hi:[1,0]
	v_pk_mul_f32 v[218:219], v[134:135], s[26:27] op_sel_hi:[1,0]
	v_pk_mul_f32 v[220:221], v[136:137], s[26:27] op_sel_hi:[1,0]
	s_cbranch_vccnz .LBB0_265
	v_and_b32_e32 v243, 64, v239
	v_xor_b32_e32 v242, 16, v239
	v_add_u32_e32 v243, 64, v243
	v_cmp_lt_i32_e32 vcc, v242, v243
	s_nop 1
	v_cndmask_b32_e32 v242, v239, v242, vcc
	v_lshlrev_b32_e32 v248, 2, v242
	ds_bpermute_b32 v242, v248, v218
	ds_bpermute_b32 v243, v248, v219
	s_waitcnt vmcnt(4) lgkmcnt(1)
	v_mul_f32_e32 v14, v14, v242
	v_cndmask_b32_e64 v14, v14, -v14, s[0:1]
	s_waitcnt vmcnt(2)
	v_fmac_f32_e32 v14, v218, v10
	ds_bpermute_b32 v10, v248, v220
	s_waitcnt lgkmcnt(1)
	v_mul_f32_e32 v15, v15, v243
	v_cndmask_b32_e64 v242, v218, v14, s[2:3]
	v_cndmask_b32_e64 v14, v15, -v15, s[0:1]
	v_fmac_f32_e32 v14, v219, v11
	ds_bpermute_b32 v11, v248, v221
	s_waitcnt lgkmcnt(1)
	v_mul_f32_e32 v10, v16, v10
	v_cndmask_b32_e64 v10, v10, -v10, s[0:1]
	v_fmac_f32_e32 v10, v220, v12
	v_cndmask_b32_e64 v244, v220, v10, s[2:3]
	s_waitcnt lgkmcnt(0)
	v_mul_f32_e32 v10, v17, v11
	ds_bpermute_b32 v11, v248, v230
	v_cndmask_b32_e64 v10, v10, -v10, s[0:1]
	v_fmac_f32_e32 v10, v221, v13
	v_cndmask_b32_e64 v245, v221, v10, s[2:3]
	ds_bpermute_b32 v10, v248, v231
	s_waitcnt lgkmcnt(1)
	v_mul_f32_e32 v6, v6, v11
	v_cndmask_b32_e64 v6, v6, -v6, s[0:1]
	v_fmac_f32_e32 v6, v230, v2
	v_cndmask_b32_e64 v246, v230, v6, s[2:3]
	s_waitcnt lgkmcnt(0)
	v_mul_f32_e32 v2, v7, v10
	v_cndmask_b32_e64 v2, v2, -v2, s[0:1]
	v_fmac_f32_e32 v2, v231, v3
	ds_bpermute_b32 v6, v248, v232
	v_cndmask_b32_e64 v247, v231, v2, s[2:3]
	ds_bpermute_b32 v2, v248, v233
	v_cndmask_b32_e64 v243, v219, v14, s[2:3]
	s_waitcnt lgkmcnt(1)
	v_mul_f32_e32 v3, v8, v6
	v_cndmask_b32_e64 v3, v3, -v3, s[0:1]
	s_waitcnt lgkmcnt(0)
	v_mul_f32_e32 v2, v9, v2
	v_cndmask_b32_e64 v2, v2, -v2, s[0:1]
	v_fmac_f32_e32 v3, v232, v4
	v_fmac_f32_e32 v2, v233, v5
	v_cndmask_b32_e64 v248, v232, v3, s[2:3]
	v_cndmask_b32_e64 v249, v233, v2, s[2:3]
	s_branch .LBB0_266

.LBB0_266:
	s_waitcnt vmcnt(2)
	v_add_u32_e32 v10, 0x800, v241
	global_load_dwordx4 v[6:9], v10, s[14:15] offset:48
	global_load_dwordx4 v[14:17], v10, s[14:15] offset:32
	global_load_dwordx4 v[2:5], v10, s[14:15] offset:16
	s_nop 0
	global_load_dwordx4 v[10:13], v10, s[14:15]
	v_lshlrev_b64 v[250:251], 1, v[226:227]
	v_lshl_add_u64 v[252:253], v[216:217], 0, v[250:251]
	v_cvt_pk_bf16_f32 v218, v218, v219
	v_cvt_pk_bf16_f32 v219, v220, v221
	v_cvt_pk_bf16_f32 v220, v230, v231
	v_cvt_pk_bf16_f32 v221, v232, v233
	global_store_dwordx4 v[252:253], v[218:221], off nt
	v_lshl_add_u64 v[230:231], v[214:215], 0, v[250:251]
	s_and_b64 vcc, exec, s[6:7]
	v_cvt_pk_bf16_f32 v218, v242, v243
	v_cvt_pk_bf16_f32 v219, v244, v245
	v_cvt_pk_bf16_f32 v220, v246, v247
	v_cvt_pk_bf16_f32 v221, v248, v249
	global_store_dwordx4 v[230:231], v[218:221], off nt
	v_pk_mul_f32 v[230:231], v[114:115], s[26:27] op_sel_hi:[1,0]
	v_pk_mul_f32 v[232:233], v[116:117], s[26:27] op_sel_hi:[1,0]
	v_pk_mul_f32 v[218:219], v[158:159], s[26:27] op_sel_hi:[1,0]
	v_pk_mul_f32 v[220:221], v[160:161], s[26:27] op_sel_hi:[1,0]
	s_cbranch_vccnz .LBB0_268
	v_and_b32_e32 v243, 64, v239
	v_xor_b32_e32 v242, 16, v239
	v_add_u32_e32 v243, 64, v243
	v_cmp_lt_i32_e32 vcc, v242, v243
	s_nop 1
	v_cndmask_b32_e32 v242, v239, v242, vcc
	v_lshlrev_b32_e32 v248, 2, v242
	ds_bpermute_b32 v242, v248, v218
	ds_bpermute_b32 v243, v248, v219
	s_waitcnt vmcnt(4) lgkmcnt(1)
	v_mul_f32_e32 v14, v14, v242
	v_cndmask_b32_e64 v14, v14, -v14, s[0:1]
	s_waitcnt vmcnt(2)
	v_fmac_f32_e32 v14, v218, v10
	ds_bpermute_b32 v10, v248, v220
	s_waitcnt lgkmcnt(1)
	v_mul_f32_e32 v15, v15, v243
	v_cndmask_b32_e64 v242, v218, v14, s[2:3]
	v_cndmask_b32_e64 v14, v15, -v15, s[0:1]
	v_fmac_f32_e32 v14, v219, v11
	ds_bpermute_b32 v11, v248, v221
	s_waitcnt lgkmcnt(1)
	v_mul_f32_e32 v10, v16, v10
	v_cndmask_b32_e64 v10, v10, -v10, s[0:1]
	v_fmac_f32_e32 v10, v220, v12
	v_cndmask_b32_e64 v244, v220, v10, s[2:3]
	s_waitcnt lgkmcnt(0)
	v_mul_f32_e32 v10, v17, v11
	ds_bpermute_b32 v11, v248, v230
	v_cndmask_b32_e64 v10, v10, -v10, s[0:1]
	v_fmac_f32_e32 v10, v221, v13
	v_cndmask_b32_e64 v245, v221, v10, s[2:3]
	ds_bpermute_b32 v10, v248, v231
	s_waitcnt lgkmcnt(1)
	v_mul_f32_e32 v6, v6, v11
	v_cndmask_b32_e64 v6, v6, -v6, s[0:1]
	v_fmac_f32_e32 v6, v230, v2
	v_cndmask_b32_e64 v246, v230, v6, s[2:3]
	s_waitcnt lgkmcnt(0)
	v_mul_f32_e32 v2, v7, v10
	v_cndmask_b32_e64 v2, v2, -v2, s[0:1]
	v_fmac_f32_e32 v2, v231, v3
	ds_bpermute_b32 v6, v248, v232
	v_cndmask_b32_e64 v247, v231, v2, s[2:3]
	ds_bpermute_b32 v2, v248, v233
	v_cndmask_b32_e64 v243, v219, v14, s[2:3]
	s_waitcnt lgkmcnt(1)
	v_mul_f32_e32 v3, v8, v6
	v_cndmask_b32_e64 v3, v3, -v3, s[0:1]
	s_waitcnt lgkmcnt(0)
	v_mul_f32_e32 v2, v9, v2
	v_cndmask_b32_e64 v2, v2, -v2, s[0:1]
	v_fmac_f32_e32 v3, v232, v4
	v_fmac_f32_e32 v2, v233, v5
	v_cndmask_b32_e64 v248, v232, v3, s[2:3]
	v_cndmask_b32_e64 v249, v233, v2, s[2:3]
	s_branch .LBB0_269

.LBB0_269:
	s_waitcnt vmcnt(2)
	v_add_u32_e32 v10, 0xc00, v241
	global_load_dwordx4 v[6:9], v10, s[14:15] offset:48
	global_load_dwordx4 v[14:17], v10, s[14:15] offset:32
	global_load_dwordx4 v[2:5], v10, s[14:15] offset:16
	s_nop 0
	global_load_dwordx4 v[10:13], v10, s[14:15]
	v_lshlrev_b64 v[250:251], 1, v[224:225]
	v_lshl_add_u64 v[252:253], v[216:217], 0, v[250:251]
	v_cvt_pk_bf16_f32 v218, v218, v219
	v_cvt_pk_bf16_f32 v219, v220, v221
	v_cvt_pk_bf16_f32 v220, v230, v231
	v_cvt_pk_bf16_f32 v221, v232, v233
	global_store_dwordx4 v[252:253], v[218:221], off nt
	v_lshl_add_u64 v[230:231], v[214:215], 0, v[250:251]
	s_and_b64 vcc, exec, s[6:7]
	v_cvt_pk_bf16_f32 v218, v242, v243
	v_cvt_pk_bf16_f32 v219, v244, v245
	v_cvt_pk_bf16_f32 v220, v246, v247
	v_cvt_pk_bf16_f32 v221, v248, v249
	global_store_dwordx4 v[230:231], v[218:221], off nt
	v_pk_mul_f32 v[230:231], v[138:139], s[26:27] op_sel_hi:[1,0]
	v_pk_mul_f32 v[232:233], v[140:141], s[26:27] op_sel_hi:[1,0]
	v_pk_mul_f32 v[218:219], v[126:127], s[26:27] op_sel_hi:[1,0]
	v_pk_mul_f32 v[220:221], v[128:129], s[26:27] op_sel_hi:[1,0]
	s_cbranch_vccnz .LBB0_271
	v_and_b32_e32 v243, 64, v239
	v_xor_b32_e32 v242, 16, v239
	v_add_u32_e32 v243, 64, v243
	v_cmp_lt_i32_e32 vcc, v242, v243
	s_nop 1
	v_cndmask_b32_e32 v242, v239, v242, vcc
	v_lshlrev_b32_e32 v248, 2, v242
	ds_bpermute_b32 v242, v248, v218
	ds_bpermute_b32 v243, v248, v219
	s_waitcnt vmcnt(4) lgkmcnt(1)
	v_mul_f32_e32 v14, v14, v242
	v_cndmask_b32_e64 v14, v14, -v14, s[0:1]
	s_waitcnt vmcnt(2)
	v_fmac_f32_e32 v14, v218, v10
	ds_bpermute_b32 v10, v248, v220
	s_waitcnt lgkmcnt(1)
	v_mul_f32_e32 v15, v15, v243
	v_cndmask_b32_e64 v242, v218, v14, s[2:3]
	v_cndmask_b32_e64 v14, v15, -v15, s[0:1]
	v_fmac_f32_e32 v14, v219, v11
	ds_bpermute_b32 v11, v248, v221
	s_waitcnt lgkmcnt(1)
	v_mul_f32_e32 v10, v16, v10
	v_cndmask_b32_e64 v10, v10, -v10, s[0:1]
	v_fmac_f32_e32 v10, v220, v12
	v_cndmask_b32_e64 v244, v220, v10, s[2:3]
	s_waitcnt lgkmcnt(0)
	v_mul_f32_e32 v10, v17, v11
	ds_bpermute_b32 v11, v248, v230
	v_cndmask_b32_e64 v10, v10, -v10, s[0:1]
	v_fmac_f32_e32 v10, v221, v13
	v_cndmask_b32_e64 v245, v221, v10, s[2:3]
	ds_bpermute_b32 v10, v248, v231
	s_waitcnt lgkmcnt(1)
	v_mul_f32_e32 v6, v6, v11
	v_cndmask_b32_e64 v6, v6, -v6, s[0:1]
	v_fmac_f32_e32 v6, v230, v2
	v_cndmask_b32_e64 v246, v230, v6, s[2:3]
	s_waitcnt lgkmcnt(0)
	v_mul_f32_e32 v2, v7, v10
	v_cndmask_b32_e64 v2, v2, -v2, s[0:1]
	v_fmac_f32_e32 v2, v231, v3
	ds_bpermute_b32 v6, v248, v232
	v_cndmask_b32_e64 v247, v231, v2, s[2:3]
	ds_bpermute_b32 v2, v248, v233
	v_cndmask_b32_e64 v243, v219, v14, s[2:3]
	s_waitcnt lgkmcnt(1)
	v_mul_f32_e32 v3, v8, v6
	v_cndmask_b32_e64 v3, v3, -v3, s[0:1]
	s_waitcnt lgkmcnt(0)
	v_mul_f32_e32 v2, v9, v2
	v_cndmask_b32_e64 v2, v2, -v2, s[0:1]
	v_fmac_f32_e32 v3, v232, v4
	v_fmac_f32_e32 v2, v233, v5
	v_cndmask_b32_e64 v248, v232, v3, s[2:3]
	v_cndmask_b32_e64 v249, v233, v2, s[2:3]
	s_branch .LBB0_272

.LBB0_272:
	s_waitcnt vmcnt(2)
	v_add_u32_e32 v10, 0x2000, v241
	global_load_dwordx4 v[6:9], v10, s[14:15] offset:48
	global_load_dwordx4 v[14:17], v10, s[14:15] offset:32
	global_load_dwordx4 v[2:5], v10, s[14:15] offset:16
	s_nop 0
	global_load_dwordx4 v[10:13], v10, s[14:15]
	v_lshlrev_b64 v[250:251], 1, v[222:223]
	v_lshl_add_u64 v[252:253], v[216:217], 0, v[250:251]
	v_cvt_pk_bf16_f32 v218, v218, v219
	v_cvt_pk_bf16_f32 v219, v220, v221
	v_cvt_pk_bf16_f32 v220, v230, v231
	v_cvt_pk_bf16_f32 v221, v232, v233
	global_store_dwordx4 v[252:253], v[218:221], off nt
	v_lshl_add_u64 v[230:231], v[214:215], 0, v[250:251]
	s_and_b64 vcc, exec, s[6:7]
	v_cvt_pk_bf16_f32 v218, v242, v243
	v_cvt_pk_bf16_f32 v219, v244, v245
	v_cvt_pk_bf16_f32 v220, v246, v247
	v_cvt_pk_bf16_f32 v221, v248, v249
	global_store_dwordx4 v[230:231], v[218:221], off nt
	v_pk_mul_f32 v[230:231], v[70:71], s[26:27] op_sel_hi:[1,0]
	v_pk_mul_f32 v[232:233], v[72:73], s[26:27] op_sel_hi:[1,0]
	v_pk_mul_f32 v[218:219], v[66:67], s[26:27] op_sel_hi:[1,0]
	v_pk_mul_f32 v[220:221], v[68:69], s[26:27] op_sel_hi:[1,0]
	s_cbranch_vccnz .LBB0_274
	v_and_b32_e32 v243, 64, v239
	v_xor_b32_e32 v242, 16, v239
	v_add_u32_e32 v243, 64, v243
	v_cmp_lt_i32_e32 vcc, v242, v243
	s_nop 1
	v_cndmask_b32_e32 v242, v239, v242, vcc
	v_lshlrev_b32_e32 v248, 2, v242
	ds_bpermute_b32 v242, v248, v218
	ds_bpermute_b32 v243, v248, v219
	s_waitcnt vmcnt(4) lgkmcnt(1)
	v_mul_f32_e32 v14, v14, v242
	v_cndmask_b32_e64 v14, v14, -v14, s[0:1]
	s_waitcnt vmcnt(2)
	v_fmac_f32_e32 v14, v218, v10
	ds_bpermute_b32 v10, v248, v220
	s_waitcnt lgkmcnt(1)
	v_mul_f32_e32 v15, v15, v243
	v_cndmask_b32_e64 v242, v218, v14, s[2:3]
	v_cndmask_b32_e64 v14, v15, -v15, s[0:1]
	v_fmac_f32_e32 v14, v219, v11
	ds_bpermute_b32 v11, v248, v221
	s_waitcnt lgkmcnt(1)
	v_mul_f32_e32 v10, v16, v10
	v_cndmask_b32_e64 v10, v10, -v10, s[0:1]
	v_fmac_f32_e32 v10, v220, v12
	v_cndmask_b32_e64 v244, v220, v10, s[2:3]
	s_waitcnt lgkmcnt(0)
	v_mul_f32_e32 v10, v17, v11
	ds_bpermute_b32 v11, v248, v230
	v_cndmask_b32_e64 v10, v10, -v10, s[0:1]
	v_fmac_f32_e32 v10, v221, v13
	v_cndmask_b32_e64 v245, v221, v10, s[2:3]
	ds_bpermute_b32 v10, v248, v231
	s_waitcnt lgkmcnt(1)
	v_mul_f32_e32 v6, v6, v11
	v_cndmask_b32_e64 v6, v6, -v6, s[0:1]
	v_fmac_f32_e32 v6, v230, v2
	v_cndmask_b32_e64 v246, v230, v6, s[2:3]
	s_waitcnt lgkmcnt(0)
	v_mul_f32_e32 v2, v7, v10
	v_cndmask_b32_e64 v2, v2, -v2, s[0:1]
	v_fmac_f32_e32 v2, v231, v3
	ds_bpermute_b32 v6, v248, v232
	v_cndmask_b32_e64 v247, v231, v2, s[2:3]
	ds_bpermute_b32 v2, v248, v233
	v_cndmask_b32_e64 v243, v219, v14, s[2:3]
	s_waitcnt lgkmcnt(1)
	v_mul_f32_e32 v3, v8, v6
	v_cndmask_b32_e64 v3, v3, -v3, s[0:1]
	s_waitcnt lgkmcnt(0)
	v_mul_f32_e32 v2, v9, v2
	v_cndmask_b32_e64 v2, v2, -v2, s[0:1]
	v_fmac_f32_e32 v3, v232, v4
	v_fmac_f32_e32 v2, v233, v5
	v_cndmask_b32_e64 v248, v232, v3, s[2:3]
	v_cndmask_b32_e64 v249, v233, v2, s[2:3]
	s_branch .LBB0_275

.LBB0_275:
	s_waitcnt vmcnt(2)
	v_add_u32_e32 v10, 0x2400, v241
	global_load_dwordx4 v[6:9], v10, s[14:15] offset:48
	global_load_dwordx4 v[14:17], v10, s[14:15] offset:32
	global_load_dwordx4 v[2:5], v10, s[14:15] offset:16
	s_nop 0
	global_load_dwordx4 v[10:13], v10, s[14:15]
	v_lshlrev_b64 v[250:251], 1, v[212:213]
	v_lshl_add_u64 v[252:253], v[216:217], 0, v[250:251]
	v_cvt_pk_bf16_f32 v218, v218, v219
	v_cvt_pk_bf16_f32 v219, v220, v221
	v_cvt_pk_bf16_f32 v220, v230, v231
	v_cvt_pk_bf16_f32 v221, v232, v233
	global_store_dwordx4 v[252:253], v[218:221], off nt
	v_lshl_add_u64 v[230:231], v[214:215], 0, v[250:251]
	s_and_b64 vcc, exec, s[6:7]
	v_cvt_pk_bf16_f32 v218, v242, v243
	v_cvt_pk_bf16_f32 v219, v244, v245
	v_cvt_pk_bf16_f32 v220, v246, v247
	v_cvt_pk_bf16_f32 v221, v248, v249
	global_store_dwordx4 v[230:231], v[218:221], off nt
	v_pk_mul_f32 v[230:231], v[78:79], s[26:27] op_sel_hi:[1,0]
	v_pk_mul_f32 v[232:233], v[80:81], s[26:27] op_sel_hi:[1,0]
	v_pk_mul_f32 v[218:219], v[74:75], s[26:27] op_sel_hi:[1,0]
	v_pk_mul_f32 v[220:221], v[76:77], s[26:27] op_sel_hi:[1,0]
	s_cbranch_vccnz .LBB0_277
	v_and_b32_e32 v243, 64, v239
	v_xor_b32_e32 v242, 16, v239
	v_add_u32_e32 v243, 64, v243
	v_cmp_lt_i32_e32 vcc, v242, v243
	s_nop 1
	v_cndmask_b32_e32 v242, v239, v242, vcc
	v_lshlrev_b32_e32 v248, 2, v242
	ds_bpermute_b32 v242, v248, v218
	ds_bpermute_b32 v243, v248, v219
	s_waitcnt vmcnt(4) lgkmcnt(1)
	v_mul_f32_e32 v14, v14, v242
	v_cndmask_b32_e64 v14, v14, -v14, s[0:1]
	s_waitcnt vmcnt(2)
	v_fmac_f32_e32 v14, v218, v10
	ds_bpermute_b32 v10, v248, v220
	s_waitcnt lgkmcnt(1)
	v_mul_f32_e32 v15, v15, v243
	v_cndmask_b32_e64 v242, v218, v14, s[2:3]
	v_cndmask_b32_e64 v14, v15, -v15, s[0:1]
	v_fmac_f32_e32 v14, v219, v11
	ds_bpermute_b32 v11, v248, v221
	s_waitcnt lgkmcnt(1)
	v_mul_f32_e32 v10, v16, v10
	v_cndmask_b32_e64 v10, v10, -v10, s[0:1]
	v_fmac_f32_e32 v10, v220, v12
	v_cndmask_b32_e64 v244, v220, v10, s[2:3]
	s_waitcnt lgkmcnt(0)
	v_mul_f32_e32 v10, v17, v11
	ds_bpermute_b32 v11, v248, v230
	v_cndmask_b32_e64 v10, v10, -v10, s[0:1]
	v_fmac_f32_e32 v10, v221, v13
	v_cndmask_b32_e64 v245, v221, v10, s[2:3]
	ds_bpermute_b32 v10, v248, v231
	s_waitcnt lgkmcnt(1)
	v_mul_f32_e32 v6, v6, v11
	v_cndmask_b32_e64 v6, v6, -v6, s[0:1]
	v_fmac_f32_e32 v6, v230, v2
	v_cndmask_b32_e64 v246, v230, v6, s[2:3]
	s_waitcnt lgkmcnt(0)
	v_mul_f32_e32 v2, v7, v10
	v_cndmask_b32_e64 v2, v2, -v2, s[0:1]
	v_fmac_f32_e32 v2, v231, v3
	ds_bpermute_b32 v6, v248, v232
	v_cndmask_b32_e64 v247, v231, v2, s[2:3]
	ds_bpermute_b32 v2, v248, v233
	v_cndmask_b32_e64 v243, v219, v14, s[2:3]
	s_waitcnt lgkmcnt(1)
	v_mul_f32_e32 v3, v8, v6
	v_cndmask_b32_e64 v3, v3, -v3, s[0:1]
	s_waitcnt lgkmcnt(0)
	v_mul_f32_e32 v2, v9, v2
	v_cndmask_b32_e64 v2, v2, -v2, s[0:1]
	v_fmac_f32_e32 v3, v232, v4
	v_fmac_f32_e32 v2, v233, v5
	v_cndmask_b32_e64 v248, v232, v3, s[2:3]
	v_cndmask_b32_e64 v249, v233, v2, s[2:3]
	s_branch .LBB0_278

.LBB0_278:
	s_waitcnt vmcnt(2)
	v_add_u32_e32 v10, 0x2800, v241
	global_load_dwordx4 v[6:9], v10, s[14:15] offset:48
	global_load_dwordx4 v[14:17], v10, s[14:15] offset:32
	global_load_dwordx4 v[2:5], v10, s[14:15] offset:16
	s_nop 0
	global_load_dwordx4 v[10:13], v10, s[14:15]
	v_lshlrev_b64 v[250:251], 1, v[210:211]
	v_lshl_add_u64 v[252:253], v[216:217], 0, v[250:251]
	v_cvt_pk_bf16_f32 v218, v218, v219
	v_cvt_pk_bf16_f32 v219, v220, v221
	v_cvt_pk_bf16_f32 v220, v230, v231
	v_cvt_pk_bf16_f32 v221, v232, v233
	global_store_dwordx4 v[252:253], v[218:221], off nt
	v_lshl_add_u64 v[230:231], v[214:215], 0, v[250:251]
	s_and_b64 vcc, exec, s[6:7]
	v_cvt_pk_bf16_f32 v218, v242, v243
	v_cvt_pk_bf16_f32 v219, v244, v245
	v_cvt_pk_bf16_f32 v220, v246, v247
	v_cvt_pk_bf16_f32 v221, v248, v249
	global_store_dwordx4 v[230:231], v[218:221], off nt
	v_pk_mul_f32 v[230:231], v[86:87], s[26:27] op_sel_hi:[1,0]
	v_pk_mul_f32 v[232:233], v[88:89], s[26:27] op_sel_hi:[1,0]
	v_pk_mul_f32 v[218:219], v[82:83], s[26:27] op_sel_hi:[1,0]
	v_pk_mul_f32 v[220:221], v[84:85], s[26:27] op_sel_hi:[1,0]
	s_cbranch_vccnz .LBB0_280
	v_and_b32_e32 v243, 64, v239
	v_xor_b32_e32 v242, 16, v239
	v_add_u32_e32 v243, 64, v243
	v_cmp_lt_i32_e32 vcc, v242, v243
	s_nop 1
	v_cndmask_b32_e32 v242, v239, v242, vcc
	v_lshlrev_b32_e32 v248, 2, v242
	ds_bpermute_b32 v242, v248, v218
	ds_bpermute_b32 v243, v248, v219
	s_waitcnt vmcnt(4) lgkmcnt(1)
	v_mul_f32_e32 v14, v14, v242
	v_cndmask_b32_e64 v14, v14, -v14, s[0:1]
	s_waitcnt vmcnt(2)
	v_fmac_f32_e32 v14, v218, v10
	ds_bpermute_b32 v10, v248, v220
	s_waitcnt lgkmcnt(1)
	v_mul_f32_e32 v15, v15, v243
	v_cndmask_b32_e64 v242, v218, v14, s[2:3]
	v_cndmask_b32_e64 v14, v15, -v15, s[0:1]
	v_fmac_f32_e32 v14, v219, v11
	ds_bpermute_b32 v11, v248, v221
	s_waitcnt lgkmcnt(1)
	v_mul_f32_e32 v10, v16, v10
	v_cndmask_b32_e64 v10, v10, -v10, s[0:1]
	v_fmac_f32_e32 v10, v220, v12
	v_cndmask_b32_e64 v244, v220, v10, s[2:3]
	s_waitcnt lgkmcnt(0)
	v_mul_f32_e32 v10, v17, v11
	ds_bpermute_b32 v11, v248, v230
	v_cndmask_b32_e64 v10, v10, -v10, s[0:1]
	v_fmac_f32_e32 v10, v221, v13
	v_cndmask_b32_e64 v245, v221, v10, s[2:3]
	ds_bpermute_b32 v10, v248, v231
	s_waitcnt lgkmcnt(1)
	v_mul_f32_e32 v6, v6, v11
	v_cndmask_b32_e64 v6, v6, -v6, s[0:1]
	v_fmac_f32_e32 v6, v230, v2
	v_cndmask_b32_e64 v246, v230, v6, s[2:3]
	s_waitcnt lgkmcnt(0)
	v_mul_f32_e32 v2, v7, v10
	v_cndmask_b32_e64 v2, v2, -v2, s[0:1]
	v_fmac_f32_e32 v2, v231, v3
	ds_bpermute_b32 v6, v248, v232
	v_cndmask_b32_e64 v247, v231, v2, s[2:3]
	ds_bpermute_b32 v2, v248, v233
	v_cndmask_b32_e64 v243, v219, v14, s[2:3]
	s_waitcnt lgkmcnt(1)
	v_mul_f32_e32 v3, v8, v6
	v_cndmask_b32_e64 v3, v3, -v3, s[0:1]
	s_waitcnt lgkmcnt(0)
	v_mul_f32_e32 v2, v9, v2
	v_cndmask_b32_e64 v2, v2, -v2, s[0:1]
	v_fmac_f32_e32 v3, v232, v4
	v_fmac_f32_e32 v2, v233, v5
	v_cndmask_b32_e64 v248, v232, v3, s[2:3]
	v_cndmask_b32_e64 v249, v233, v2, s[2:3]
	s_branch .LBB0_281

.LBB0_281:
	s_waitcnt vmcnt(2)
	v_add_u32_e32 v10, 0x2c00, v241
	global_load_dwordx4 v[6:9], v10, s[14:15] offset:48
	global_load_dwordx4 v[14:17], v10, s[14:15] offset:32
	global_load_dwordx4 v[2:5], v10, s[14:15] offset:16
	s_nop 0
	global_load_dwordx4 v[10:13], v10, s[14:15]
	v_lshlrev_b64 v[250:251], 1, v[208:209]
	v_lshl_add_u64 v[252:253], v[216:217], 0, v[250:251]
	v_cvt_pk_bf16_f32 v218, v218, v219
	v_cvt_pk_bf16_f32 v219, v220, v221
	v_cvt_pk_bf16_f32 v220, v230, v231
	v_cvt_pk_bf16_f32 v221, v232, v233
	global_store_dwordx4 v[252:253], v[218:221], off nt
	v_lshl_add_u64 v[230:231], v[214:215], 0, v[250:251]
	s_and_b64 vcc, exec, s[6:7]
	v_cvt_pk_bf16_f32 v218, v242, v243
	v_cvt_pk_bf16_f32 v219, v244, v245
	v_cvt_pk_bf16_f32 v220, v246, v247
	v_cvt_pk_bf16_f32 v221, v248, v249
	global_store_dwordx4 v[230:231], v[218:221], off nt
	v_pk_mul_f32 v[230:231], v[94:95], s[26:27] op_sel_hi:[1,0]
	v_pk_mul_f32 v[232:233], v[96:97], s[26:27] op_sel_hi:[1,0]
	v_pk_mul_f32 v[218:219], v[90:91], s[26:27] op_sel_hi:[1,0]
	v_pk_mul_f32 v[220:221], v[92:93], s[26:27] op_sel_hi:[1,0]
	s_cbranch_vccnz .LBB0_283
	v_and_b32_e32 v242, 64, v239
	v_xor_b32_e32 v241, 16, v239
	v_add_u32_e32 v242, 64, v242
	v_cmp_lt_i32_e32 vcc, v241, v242
	s_nop 1
	v_cndmask_b32_e32 v241, v239, v241, vcc
	v_lshlrev_b32_e32 v241, 2, v241
	ds_bpermute_b32 v242, v241, v218
	ds_bpermute_b32 v243, v241, v219
	s_waitcnt vmcnt(4) lgkmcnt(1)
	v_mul_f32_e32 v14, v14, v242
	v_cndmask_b32_e64 v14, v14, -v14, s[0:1]
	s_waitcnt vmcnt(2)
	v_fmac_f32_e32 v14, v218, v10
	s_waitcnt lgkmcnt(0)
	v_mul_f32_e32 v15, v15, v243
	v_cndmask_b32_e64 v10, v218, v14, s[2:3]
	ds_bpermute_b32 v14, v241, v220
	v_cndmask_b32_e64 v15, v15, -v15, s[0:1]
	v_fmac_f32_e32 v15, v219, v11
	v_cndmask_b32_e64 v11, v219, v15, s[2:3]
	ds_bpermute_b32 v15, v241, v221
	s_waitcnt lgkmcnt(1)
	v_mul_f32_e32 v14, v16, v14
	v_cndmask_b32_e64 v14, v14, -v14, s[0:1]
	v_fmac_f32_e32 v14, v220, v12
	v_cndmask_b32_e64 v12, v220, v14, s[2:3]
	s_waitcnt lgkmcnt(0)
	v_mul_f32_e32 v14, v17, v15
	ds_bpermute_b32 v15, v241, v230
	v_cndmask_b32_e64 v14, v14, -v14, s[0:1]
	v_fmac_f32_e32 v14, v221, v13
	v_cndmask_b32_e64 v13, v221, v14, s[2:3]
	ds_bpermute_b32 v14, v241, v231
	s_waitcnt lgkmcnt(1)
	v_mul_f32_e32 v6, v6, v15
	v_cndmask_b32_e64 v6, v6, -v6, s[0:1]
	v_fmac_f32_e32 v6, v230, v2
	v_cndmask_b32_e64 v2, v230, v6, s[2:3]
	s_waitcnt lgkmcnt(0)
	v_mul_f32_e32 v6, v7, v14
	v_cndmask_b32_e64 v6, v6, -v6, s[0:1]
	v_fmac_f32_e32 v6, v231, v3
	ds_bpermute_b32 v7, v241, v232
	v_cndmask_b32_e64 v3, v231, v6, s[2:3]
	ds_bpermute_b32 v6, v241, v233
	s_waitcnt lgkmcnt(1)
	v_mul_f32_e32 v7, v8, v7
	v_cndmask_b32_e64 v7, v7, -v7, s[0:1]
	s_waitcnt lgkmcnt(0)
	v_mul_f32_e32 v6, v9, v6
	v_cndmask_b32_e64 v6, v6, -v6, s[0:1]
	v_fmac_f32_e32 v7, v232, v4
	v_fmac_f32_e32 v6, v233, v5
	v_cndmask_b32_e64 v4, v232, v7, s[2:3]
	v_cndmask_b32_e64 v5, v233, v6, s[2:3]
	s_branch .LBB0_284

.LBB0_284:
	v_lshlrev_b64 v[14:15], 1, v[206:207]
	v_lshl_add_u64 v[16:17], v[216:217], 0, v[14:15]
	v_cvt_pk_bf16_f32 v6, v218, v219
	v_cvt_pk_bf16_f32 v7, v220, v221
	v_cvt_pk_bf16_f32 v8, v230, v231
	v_cvt_pk_bf16_f32 v9, v232, v233
	global_store_dwordx4 v[16:17], v[6:9], off nt
	v_lshl_add_u64 v[14:15], v[214:215], 0, v[14:15]
	s_nop 0
	v_cvt_pk_bf16_f32 v6, v10, v11
	v_cvt_pk_bf16_f32 v7, v12, v13
	v_cvt_pk_bf16_f32 v8, v2, v3
	v_cvt_pk_bf16_f32 v9, v4, v5
	global_store_dwordx4 v[14:15], v[6:9], off nt
	s_or_b32 s31, s29, 1
	s_cmp_lt_i32 s31, 4
	s_mov_b64 s[42:43], -1
	s_cbranch_scc1 .LBB0_258
.LBB0_285:
	s_cmp_lt_u32 s29, 10
	s_cbranch_scc1 .LBB0_297
	s_cmp_lt_u32 s29, 14
	s_cbranch_scc1 .LBB0_294
	s_cmp_lt_u32 s29, 22
	s_cbranch_scc1 .LBB0_291
	s_cmp_gt_u32 s29, 37
	s_cbranch_scc1 .LBB0_290
	v_mul_f32_e32 v8, 0xbfb8aa3b, v166
	v_exp_f32_e32 v8, v8
	v_mul_f32_e32 v9, 0xbfb8aa3b, v167
	v_exp_f32_e32 v9, v9
	v_mul_f32_e32 v4, 0xbfb8aa3b, v162
	v_add_f32_e32 v8, 1.0, v8
	s_waitcnt vmcnt(0)
	v_rcp_f32_e32 v10, v8
	v_add_f32_e32 v8, 1.0, v9
	v_mul_f32_e32 v9, 0xbfb8aa3b, v168
	v_mul_f32_e32 v5, 0xbfb8aa3b, v163
	v_mul_f32_e32 v6, 0xbfb8aa3b, v164
	v_mul_f32_e32 v7, 0xbfb8aa3b, v165
	v_exp_f32_e32 v9, v9
	v_mul_f32_e32 v11, 0xbfb8aa3b, v169
	s_sub_i32 s33, s29, 21
	v_exp_f32_e32 v4, v4
	v_exp_f32_e32 v5, v5
	v_exp_f32_e32 v6, v6
	v_exp_f32_e32 v7, v7
	v_exp_f32_e32 v11, v11
	s_lshr_b32 s8, s33, 3
	s_lshl_b64 s[42:43], s[8:9], 26
	s_add_u32 s8, s80, s42
	v_rcp_f32_e32 v12, v8
	v_add_f32_e32 v8, 1.0, v9
	s_addc_u32 s43, s81, s43
	s_lshl_b32 s33, s33, 8
	v_add_f32_e32 v4, 1.0, v4
	v_add_f32_e32 v5, 1.0, v5
	v_add_f32_e32 v6, 1.0, v6
	v_add_f32_e32 v7, 1.0, v7
	v_rcp_f32_e32 v13, v8
	v_add_f32_e32 v8, 1.0, v11
	s_and_b32 s33, s33, 0x700
	v_mov_b32_e32 v2, v235
	v_mov_b32_e32 v3, v240
	v_rcp_f32_e32 v4, v4
	v_rcp_f32_e32 v5, v5
	v_rcp_f32_e32 v6, v6
	v_rcp_f32_e32 v7, v7
	v_rcp_f32_e32 v11, v8
	s_add_u32 s42, s8, s33
	s_addc_u32 s43, s43, 0
	v_ashrrev_i32_e32 v3, 31, v2
	v_lshl_add_u64 v[2:3], v[2:3], 1, s[42:43]
	v_lshl_add_u64 v[8:9], v[2:3], 0, v[64:65]
	v_cvt_pk_bf16_f32 v4, v4, v5
	v_cvt_pk_bf16_f32 v5, v6, v7
	v_cvt_pk_bf16_f32 v6, v10, v12
	v_cvt_pk_bf16_f32 v7, v13, v11
	global_store_dwordx4 v[8:9], v[4:7], off nt
	v_mul_f32_e32 v8, 0xbfb8aa3b, v174
	v_mul_f32_e32 v10, 0xbfb8aa3b, v170
	v_exp_f32_e32 v8, v8
	v_mul_f32_e32 v9, 0xbfb8aa3b, v175
	v_exp_f32_e32 v10, v10
	v_mul_f32_e32 v11, 0xbfb8aa3b, v171
	v_exp_f32_e32 v9, v9
	v_exp_f32_e32 v11, v11
	v_add_f32_e32 v8, 1.0, v8
	v_add_f32_e32 v4, 1.0, v10
	v_rcp_f32_e32 v10, v8
	v_add_f32_e32 v8, 1.0, v9
	v_mul_f32_e32 v9, 0xbfb8aa3b, v176
	v_add_f32_e32 v5, 1.0, v11
	v_mul_f32_e32 v6, 0xbfb8aa3b, v172
	v_mul_f32_e32 v7, 0xbfb8aa3b, v173
	v_exp_f32_e32 v9, v9
	v_mul_f32_e32 v11, 0xbfb8aa3b, v177
	v_exp_f32_e32 v6, v6
	v_exp_f32_e32 v7, v7
	v_exp_f32_e32 v11, v11
	v_rcp_f32_e32 v12, v8
	v_add_f32_e32 v8, 1.0, v9
	v_add_f32_e32 v6, 1.0, v6
	v_add_f32_e32 v7, 1.0, v7
	v_rcp_f32_e32 v13, v8
	v_add_f32_e32 v8, 1.0, v11
	v_rcp_f32_e32 v4, v4
	v_rcp_f32_e32 v5, v5
	v_rcp_f32_e32 v6, v6
	v_rcp_f32_e32 v7, v7
	v_rcp_f32_e32 v11, v8
	v_lshl_add_u64 v[8:9], v[2:3], 0, v[62:63]
	v_cvt_pk_bf16_f32 v4, v4, v5
	v_cvt_pk_bf16_f32 v5, v6, v7
	v_cvt_pk_bf16_f32 v6, v10, v12
	v_cvt_pk_bf16_f32 v7, v13, v11
	global_store_dwordx4 v[8:9], v[4:7], off nt
	v_mul_f32_e32 v8, 0xbfb8aa3b, v182
	v_mul_f32_e32 v10, 0xbfb8aa3b, v178
	v_exp_f32_e32 v8, v8
	v_mul_f32_e32 v9, 0xbfb8aa3b, v183
	v_exp_f32_e32 v10, v10
	v_mul_f32_e32 v11, 0xbfb8aa3b, v179
	v_exp_f32_e32 v9, v9
	v_exp_f32_e32 v11, v11
	v_add_f32_e32 v8, 1.0, v8
	v_add_f32_e32 v4, 1.0, v10
	v_rcp_f32_e32 v10, v8
	v_add_f32_e32 v8, 1.0, v9
	v_mul_f32_e32 v9, 0xbfb8aa3b, v184
	v_add_f32_e32 v5, 1.0, v11
	v_mul_f32_e32 v6, 0xbfb8aa3b, v180
	v_mul_f32_e32 v7, 0xbfb8aa3b, v181
	v_exp_f32_e32 v9, v9
	v_mul_f32_e32 v11, 0xbfb8aa3b, v185
	v_exp_f32_e32 v6, v6
	v_exp_f32_e32 v7, v7
	v_exp_f32_e32 v11, v11
	v_rcp_f32_e32 v12, v8
	v_add_f32_e32 v8, 1.0, v9
	v_add_f32_e32 v6, 1.0, v6
	v_add_f32_e32 v7, 1.0, v7
	v_rcp_f32_e32 v13, v8
	v_add_f32_e32 v8, 1.0, v11
	v_rcp_f32_e32 v4, v4
	v_rcp_f32_e32 v5, v5
	v_rcp_f32_e32 v6, v6
	v_rcp_f32_e32 v7, v7
	v_rcp_f32_e32 v11, v8
	v_lshl_add_u64 v[8:9], v[2:3], 0, v[60:61]
	v_cvt_pk_bf16_f32 v4, v4, v5
	v_cvt_pk_bf16_f32 v5, v6, v7
	v_cvt_pk_bf16_f32 v6, v10, v12
	v_cvt_pk_bf16_f32 v7, v13, v11
	global_store_dwordx4 v[8:9], v[4:7], off nt
	v_mul_f32_e32 v8, 0xbfb8aa3b, v190
	v_mul_f32_e32 v10, 0xbfb8aa3b, v186
	v_exp_f32_e32 v8, v8
	v_mul_f32_e32 v9, 0xbfb8aa3b, v191
	v_exp_f32_e32 v10, v10
	v_mul_f32_e32 v11, 0xbfb8aa3b, v187
	v_exp_f32_e32 v9, v9
	v_exp_f32_e32 v11, v11
	v_add_f32_e32 v8, 1.0, v8
	v_add_f32_e32 v4, 1.0, v10
	v_rcp_f32_e32 v10, v8
	v_add_f32_e32 v8, 1.0, v9
	v_mul_f32_e32 v9, 0xbfb8aa3b, v192
	v_add_f32_e32 v5, 1.0, v11
	v_mul_f32_e32 v6, 0xbfb8aa3b, v188
	v_mul_f32_e32 v7, 0xbfb8aa3b, v189
	v_exp_f32_e32 v9, v9
	v_mul_f32_e32 v11, 0xbfb8aa3b, v193
	v_exp_f32_e32 v6, v6
	v_exp_f32_e32 v7, v7
	v_exp_f32_e32 v11, v11
	v_rcp_f32_e32 v12, v8
	v_add_f32_e32 v8, 1.0, v9
	v_add_f32_e32 v6, 1.0, v6
	v_add_f32_e32 v7, 1.0, v7
	v_rcp_f32_e32 v13, v8
	v_add_f32_e32 v8, 1.0, v11
	v_rcp_f32_e32 v4, v4
	v_rcp_f32_e32 v5, v5
	v_rcp_f32_e32 v6, v6
	v_rcp_f32_e32 v7, v7
	v_rcp_f32_e32 v11, v8
	v_lshl_add_u64 v[8:9], v[2:3], 0, v[58:59]
	v_cvt_pk_bf16_f32 v4, v4, v5
	v_cvt_pk_bf16_f32 v5, v6, v7
	v_cvt_pk_bf16_f32 v6, v10, v12
	v_cvt_pk_bf16_f32 v7, v13, v11
	global_store_dwordx4 v[8:9], v[4:7], off nt
	v_mul_f32_e32 v8, 0xbfb8aa3b, v102
	v_mul_f32_e32 v10, 0xbfb8aa3b, v98
	v_exp_f32_e32 v8, v8
	v_mul_f32_e32 v9, 0xbfb8aa3b, v103
	v_exp_f32_e32 v10, v10
	v_mul_f32_e32 v11, 0xbfb8aa3b, v99
	v_exp_f32_e32 v9, v9
	v_exp_f32_e32 v11, v11
	v_add_f32_e32 v8, 1.0, v8
	v_add_f32_e32 v4, 1.0, v10
	v_rcp_f32_e32 v10, v8
	v_add_f32_e32 v8, 1.0, v9
	v_mul_f32_e32 v9, 0xbfb8aa3b, v104
	v_add_f32_e32 v5, 1.0, v11
	v_mul_f32_e32 v6, 0xbfb8aa3b, v100
	v_mul_f32_e32 v7, 0xbfb8aa3b, v101
	v_exp_f32_e32 v9, v9
	v_mul_f32_e32 v11, 0xbfb8aa3b, v105
	v_exp_f32_e32 v6, v6
	v_exp_f32_e32 v7, v7
	v_exp_f32_e32 v11, v11
	v_rcp_f32_e32 v12, v8
	v_add_f32_e32 v8, 1.0, v9
	v_add_f32_e32 v6, 1.0, v6
	v_add_f32_e32 v7, 1.0, v7
	v_rcp_f32_e32 v13, v8
	v_add_f32_e32 v8, 1.0, v11
	v_rcp_f32_e32 v4, v4
	v_rcp_f32_e32 v5, v5
	v_rcp_f32_e32 v6, v6
	v_rcp_f32_e32 v7, v7
	v_rcp_f32_e32 v11, v8
	v_lshl_add_u64 v[8:9], v[2:3], 0, v[56:57]
	v_cvt_pk_bf16_f32 v4, v4, v5
	v_cvt_pk_bf16_f32 v5, v6, v7
	v_cvt_pk_bf16_f32 v6, v10, v12
	v_cvt_pk_bf16_f32 v7, v13, v11
	global_store_dwordx4 v[8:9], v[4:7], off nt
	v_mul_f32_e32 v8, 0xbfb8aa3b, v118
	v_mul_f32_e32 v10, 0xbfb8aa3b, v110
	v_exp_f32_e32 v8, v8
	v_mul_f32_e32 v9, 0xbfb8aa3b, v119
	v_exp_f32_e32 v10, v10
	v_mul_f32_e32 v11, 0xbfb8aa3b, v111
	v_exp_f32_e32 v9, v9
	v_exp_f32_e32 v11, v11
	v_add_f32_e32 v8, 1.0, v8
	v_add_f32_e32 v4, 1.0, v10
	v_rcp_f32_e32 v10, v8
	v_add_f32_e32 v8, 1.0, v9
	v_mul_f32_e32 v9, 0xbfb8aa3b, v120
	v_add_f32_e32 v5, 1.0, v11
	v_mul_f32_e32 v6, 0xbfb8aa3b, v112
	v_mul_f32_e32 v7, 0xbfb8aa3b, v113
	v_exp_f32_e32 v9, v9
	v_mul_f32_e32 v11, 0xbfb8aa3b, v121
	v_exp_f32_e32 v6, v6
	v_exp_f32_e32 v7, v7
	v_exp_f32_e32 v11, v11
	v_rcp_f32_e32 v12, v8
	v_add_f32_e32 v8, 1.0, v9
	v_add_f32_e32 v6, 1.0, v6
	v_add_f32_e32 v7, 1.0, v7
	v_rcp_f32_e32 v13, v8
	v_add_f32_e32 v8, 1.0, v11
	v_rcp_f32_e32 v4, v4
	v_rcp_f32_e32 v5, v5
	v_rcp_f32_e32 v6, v6
	v_rcp_f32_e32 v7, v7
	v_rcp_f32_e32 v11, v8
	v_lshl_add_u64 v[8:9], v[2:3], 0, v[54:55]
	v_cvt_pk_bf16_f32 v4, v4, v5
	v_cvt_pk_bf16_f32 v5, v6, v7
	v_cvt_pk_bf16_f32 v6, v10, v12
	v_cvt_pk_bf16_f32 v7, v13, v11
	global_store_dwordx4 v[8:9], v[4:7], off nt
	v_mul_f32_e32 v8, 0xbfb8aa3b, v142
	v_mul_f32_e32 v10, 0xbfb8aa3b, v130
	v_exp_f32_e32 v8, v8
	v_mul_f32_e32 v9, 0xbfb8aa3b, v143
	v_exp_f32_e32 v10, v10
	v_mul_f32_e32 v11, 0xbfb8aa3b, v131
	v_exp_f32_e32 v9, v9
	v_exp_f32_e32 v11, v11
	v_add_f32_e32 v8, 1.0, v8
	v_add_f32_e32 v4, 1.0, v10
	v_rcp_f32_e32 v10, v8
	v_add_f32_e32 v8, 1.0, v9
	v_mul_f32_e32 v9, 0xbfb8aa3b, v144
	v_add_f32_e32 v5, 1.0, v11
	v_mul_f32_e32 v6, 0xbfb8aa3b, v132
	v_mul_f32_e32 v7, 0xbfb8aa3b, v133
	v_exp_f32_e32 v9, v9
	v_mul_f32_e32 v11, 0xbfb8aa3b, v145
	v_exp_f32_e32 v6, v6
	v_exp_f32_e32 v7, v7
	v_exp_f32_e32 v11, v11
	v_rcp_f32_e32 v12, v8
	v_add_f32_e32 v8, 1.0, v9
	v_add_f32_e32 v6, 1.0, v6
	v_add_f32_e32 v7, 1.0, v7
	v_rcp_f32_e32 v13, v8
	v_add_f32_e32 v8, 1.0, v11
	v_rcp_f32_e32 v4, v4
	v_rcp_f32_e32 v5, v5
	v_rcp_f32_e32 v6, v6
	v_rcp_f32_e32 v7, v7
	v_rcp_f32_e32 v11, v8
	v_lshl_add_u64 v[8:9], v[2:3], 0, v[52:53]
	v_cvt_pk_bf16_f32 v4, v4, v5
	v_cvt_pk_bf16_f32 v5, v6, v7
	v_cvt_pk_bf16_f32 v6, v10, v12
	v_cvt_pk_bf16_f32 v7, v13, v11
	global_store_dwordx4 v[8:9], v[4:7], off nt
	v_mul_f32_e32 v10, 0xbfb8aa3b, v150
	v_exp_f32_e32 v10, v10
	v_mul_f32_e32 v6, 0xbfb8aa3b, v152
	v_exp_f32_e32 v6, v6
	v_mul_f32_e32 v7, 0xbfb8aa3b, v153
	v_exp_f32_e32 v7, v7
	v_mul_f32_e32 v11, 0xbfb8aa3b, v151
	v_add_f32_e32 v6, 1.0, v6
	v_rcp_f32_e32 v8, v6
	v_add_f32_e32 v6, 1.0, v7
	v_mul_f32_e32 v7, 0xbfb8aa3b, v154
	v_exp_f32_e32 v7, v7
	v_mul_f32_e32 v9, 0xbfb8aa3b, v155
	v_exp_f32_e32 v11, v11
	v_exp_f32_e32 v9, v9
	v_add_f32_e32 v4, 1.0, v10
	v_rcp_f32_e32 v10, v6
	v_add_f32_e32 v6, 1.0, v7
	v_mul_f32_e32 v7, 0xbfb8aa3b, v156
	v_add_f32_e32 v5, 1.0, v11
	v_rcp_f32_e32 v11, v6
	v_add_f32_e32 v6, 1.0, v9
	v_exp_f32_e32 v7, v7
	v_mul_f32_e32 v9, 0xbfb8aa3b, v157
	v_exp_f32_e32 v9, v9
	v_rcp_f32_e32 v12, v6
	v_add_f32_e32 v6, 1.0, v7
	v_rcp_f32_e32 v13, v6
	v_add_f32_e32 v6, 1.0, v9
	v_rcp_f32_e32 v4, v4
	v_rcp_f32_e32 v5, v5
	v_rcp_f32_e32 v9, v6
	v_lshl_add_u64 v[6:7], v[2:3], 0, v[50:51]
	v_cvt_pk_bf16_f32 v3, v8, v10
	v_cvt_pk_bf16_f32 v2, v4, v5
	v_cvt_pk_bf16_f32 v4, v11, v12
	v_cvt_pk_bf16_f32 v5, v13, v9
	global_store_dwordx4 v[6:7], v[2:5], off nt

.LBB0_291:
	s_andn2_b64 vcc, exec, s[42:43]
	s_cbranch_vccnz .LBB0_293
	s_add_i32 s33, s29, -9
	s_lshr_b32 s8, s33, 2
	s_lshl_b64 s[42:43], s[8:9], 25
	s_add_u32 s8, s76, s42
	s_addc_u32 s43, s77, s43
	s_lshl_b32 s33, s33, 8
	s_and_b32 s33, s33, 0x300
	v_mov_b32_e32 v2, v235
	v_mov_b32_e32 v3, v240
	s_add_u32 s42, s8, s33
	s_addc_u32 s43, s43, 0
	v_ashrrev_i32_e32 v3, 31, v2
	v_lshl_add_u64 v[6:7], v[2:3], 1, s[42:43]
	v_lshl_add_u64 v[8:9], v[6:7], 0, v[48:49]
	v_cvt_pk_bf16_f32 v2, v162, v163
	v_cvt_pk_bf16_f32 v3, v164, v165
	v_cvt_pk_bf16_f32 v4, v166, v167
	v_cvt_pk_bf16_f32 v5, v168, v169
	global_store_dwordx4 v[8:9], v[2:5], off nt
	v_lshl_add_u64 v[8:9], v[6:7], 0, v[46:47]
	s_nop 0
	v_cvt_pk_bf16_f32 v2, v170, v171
	v_cvt_pk_bf16_f32 v3, v172, v173
	v_cvt_pk_bf16_f32 v4, v174, v175
	v_cvt_pk_bf16_f32 v5, v176, v177
	global_store_dwordx4 v[8:9], v[2:5], off nt
	v_lshl_add_u64 v[8:9], v[6:7], 0, v[44:45]
	s_nop 0
	v_cvt_pk_bf16_f32 v2, v178, v179
	v_cvt_pk_bf16_f32 v3, v180, v181
	v_cvt_pk_bf16_f32 v4, v182, v183
	v_cvt_pk_bf16_f32 v5, v184, v185
	global_store_dwordx4 v[8:9], v[2:5], off nt
	v_lshl_add_u64 v[8:9], v[6:7], 0, v[42:43]
	s_nop 0
	v_cvt_pk_bf16_f32 v2, v186, v187
	v_cvt_pk_bf16_f32 v3, v188, v189
	v_cvt_pk_bf16_f32 v4, v190, v191
	v_cvt_pk_bf16_f32 v5, v192, v193
	global_store_dwordx4 v[8:9], v[2:5], off nt
	v_lshl_add_u64 v[8:9], v[6:7], 0, v[40:41]
	s_nop 0
	v_cvt_pk_bf16_f32 v2, v98, v99
	v_cvt_pk_bf16_f32 v3, v100, v101
	v_cvt_pk_bf16_f32 v4, v102, v103
	v_cvt_pk_bf16_f32 v5, v104, v105
	global_store_dwordx4 v[8:9], v[2:5], off nt
	v_lshl_add_u64 v[8:9], v[6:7], 0, v[38:39]
	s_nop 0
	v_cvt_pk_bf16_f32 v2, v110, v111
	v_cvt_pk_bf16_f32 v3, v112, v113
	v_cvt_pk_bf16_f32 v4, v118, v119
	v_cvt_pk_bf16_f32 v5, v120, v121
	global_store_dwordx4 v[8:9], v[2:5], off nt
	v_lshl_add_u64 v[8:9], v[6:7], 0, v[36:37]
	v_lshl_add_u64 v[6:7], v[6:7], 0, v[34:35]
	v_cvt_pk_bf16_f32 v2, v130, v131
	v_cvt_pk_bf16_f32 v3, v132, v133
	v_cvt_pk_bf16_f32 v4, v142, v143
	v_cvt_pk_bf16_f32 v5, v144, v145
	global_store_dwordx4 v[8:9], v[2:5], off nt
	s_nop 1
	v_cvt_pk_bf16_f32 v2, v150, v151
	v_cvt_pk_bf16_f32 v3, v152, v153
	v_cvt_pk_bf16_f32 v4, v154, v155
	v_cvt_pk_bf16_f32 v5, v156, v157
	global_store_dwordx4 v[6:7], v[2:5], off nt

.LBB0_294:
	s_andn2_b64 vcc, exec, s[42:43]
	s_cbranch_vccnz .LBB0_296
	s_lshl_b32 s8, s31, 8
	v_mov_b32_e32 v2, v235
	v_mov_b32_e32 v3, v240
	s_add_u32 s42, s76, s8
	s_addc_u32 s43, s77, 0
	v_ashrrev_i32_e32 v3, 31, v2
	v_lshl_add_u64 v[6:7], v[2:3], 1, s[42:43]
	v_pk_mul_f32 v[2:3], v[162:163], s[26:27] op_sel_hi:[1,0]
	v_pk_mul_f32 v[4:5], v[164:165], s[26:27] op_sel_hi:[1,0]
	v_pk_mul_f32 v[8:9], v[166:167], s[26:27] op_sel_hi:[1,0]
	s_waitcnt vmcnt(0)
	v_pk_mul_f32 v[10:11], v[168:169], s[26:27] op_sel_hi:[1,0]
	v_lshl_add_u64 v[12:13], v[6:7], 0, v[48:49]
	v_cvt_pk_bf16_f32 v2, v2, v3
	v_cvt_pk_bf16_f32 v3, v4, v5
	v_cvt_pk_bf16_f32 v4, v8, v9
	v_cvt_pk_bf16_f32 v5, v10, v11
	global_store_dwordx4 v[12:13], v[2:5], off offset:-2560 nt
	v_pk_mul_f32 v[8:9], v[174:175], s[26:27] op_sel_hi:[1,0]
	v_pk_mul_f32 v[10:11], v[176:177], s[26:27] op_sel_hi:[1,0]
	v_pk_mul_f32 v[2:3], v[170:171], s[26:27] op_sel_hi:[1,0]
	v_pk_mul_f32 v[4:5], v[172:173], s[26:27] op_sel_hi:[1,0]
	v_lshl_add_u64 v[12:13], v[6:7], 0, v[46:47]
	v_cvt_pk_bf16_f32 v2, v2, v3
	v_cvt_pk_bf16_f32 v3, v4, v5
	v_cvt_pk_bf16_f32 v4, v8, v9
	v_cvt_pk_bf16_f32 v5, v10, v11
	global_store_dwordx4 v[12:13], v[2:5], off offset:-2560 nt
	v_pk_mul_f32 v[8:9], v[182:183], s[26:27] op_sel_hi:[1,0]
	v_pk_mul_f32 v[10:11], v[184:185], s[26:27] op_sel_hi:[1,0]
	v_pk_mul_f32 v[2:3], v[178:179], s[26:27] op_sel_hi:[1,0]
	v_pk_mul_f32 v[4:5], v[180:181], s[26:27] op_sel_hi:[1,0]
	v_lshl_add_u64 v[12:13], v[6:7], 0, v[44:45]
	v_cvt_pk_bf16_f32 v2, v2, v3
	v_cvt_pk_bf16_f32 v3, v4, v5
	v_cvt_pk_bf16_f32 v4, v8, v9
	v_cvt_pk_bf16_f32 v5, v10, v11
	global_store_dwordx4 v[12:13], v[2:5], off offset:-2560 nt
	v_pk_mul_f32 v[8:9], v[190:191], s[26:27] op_sel_hi:[1,0]
	v_pk_mul_f32 v[10:11], v[192:193], s[26:27] op_sel_hi:[1,0]
	v_pk_mul_f32 v[2:3], v[186:187], s[26:27] op_sel_hi:[1,0]
	v_pk_mul_f32 v[4:5], v[188:189], s[26:27] op_sel_hi:[1,0]
	v_lshl_add_u64 v[12:13], v[6:7], 0, v[42:43]
	v_cvt_pk_bf16_f32 v2, v2, v3
	v_cvt_pk_bf16_f32 v3, v4, v5
	v_cvt_pk_bf16_f32 v4, v8, v9
	v_cvt_pk_bf16_f32 v5, v10, v11
	global_store_dwordx4 v[12:13], v[2:5], off offset:-2560 nt
	v_pk_mul_f32 v[8:9], v[102:103], s[26:27] op_sel_hi:[1,0]
	v_pk_mul_f32 v[10:11], v[104:105], s[26:27] op_sel_hi:[1,0]
	v_pk_mul_f32 v[2:3], v[98:99], s[26:27] op_sel_hi:[1,0]
	v_pk_mul_f32 v[4:5], v[100:101], s[26:27] op_sel_hi:[1,0]
	v_lshl_add_u64 v[12:13], v[6:7], 0, v[40:41]
	v_cvt_pk_bf16_f32 v2, v2, v3
	v_cvt_pk_bf16_f32 v3, v4, v5
	v_cvt_pk_bf16_f32 v4, v8, v9
	v_cvt_pk_bf16_f32 v5, v10, v11
	global_store_dwordx4 v[12:13], v[2:5], off offset:-2560 nt
	v_pk_mul_f32 v[8:9], v[118:119], s[26:27] op_sel_hi:[1,0]
	v_pk_mul_f32 v[10:11], v[120:121], s[26:27] op_sel_hi:[1,0]
	v_pk_mul_f32 v[2:3], v[110:111], s[26:27] op_sel_hi:[1,0]
	v_pk_mul_f32 v[4:5], v[112:113], s[26:27] op_sel_hi:[1,0]
	v_lshl_add_u64 v[12:13], v[6:7], 0, v[38:39]
	v_cvt_pk_bf16_f32 v2, v2, v3
	v_cvt_pk_bf16_f32 v3, v4, v5
	v_cvt_pk_bf16_f32 v4, v8, v9
	v_cvt_pk_bf16_f32 v5, v10, v11
	global_store_dwordx4 v[12:13], v[2:5], off offset:-2560 nt
	v_pk_mul_f32 v[8:9], v[142:143], s[26:27] op_sel_hi:[1,0]
	v_pk_mul_f32 v[10:11], v[144:145], s[26:27] op_sel_hi:[1,0]
	v_pk_mul_f32 v[2:3], v[130:131], s[26:27] op_sel_hi:[1,0]
	v_pk_mul_f32 v[4:5], v[132:133], s[26:27] op_sel_hi:[1,0]
	v_lshl_add_u64 v[12:13], v[6:7], 0, v[36:37]
	v_cvt_pk_bf16_f32 v2, v2, v3
	v_cvt_pk_bf16_f32 v3, v4, v5
	v_cvt_pk_bf16_f32 v4, v8, v9
	v_cvt_pk_bf16_f32 v5, v10, v11
	global_store_dwordx4 v[12:13], v[2:5], off offset:-2560 nt
	v_pk_mul_f32 v[8:9], v[154:155], s[26:27] op_sel_hi:[1,0]
	v_pk_mul_f32 v[10:11], v[156:157], s[26:27] op_sel_hi:[1,0]
	v_pk_mul_f32 v[2:3], v[150:151], s[26:27] op_sel_hi:[1,0]
	v_pk_mul_f32 v[4:5], v[152:153], s[26:27] op_sel_hi:[1,0]
	v_lshl_add_u64 v[6:7], v[6:7], 0, v[34:35]
	v_cvt_pk_bf16_f32 v2, v2, v3
	v_cvt_pk_bf16_f32 v3, v4, v5
	v_cvt_pk_bf16_f32 v4, v8, v9
	v_cvt_pk_bf16_f32 v5, v10, v11
	global_store_dwordx4 v[6:7], v[2:5], off offset:-2560 nt

.LBB0_297:
	s_andn2_b64 vcc, exec, s[42:43]
	s_cbranch_vccnz .LBB0_299
	s_add_i32 s8, s29, -3
	s_lshl_b64 s[42:43], s[8:9], 23
	v_mov_b32_e32 v2, v235
	v_mov_b32_e32 v3, v240
	s_add_u32 s42, s74, s42
	s_addc_u32 s43, s75, s43
	v_ashrrev_i32_e32 v3, 31, v2
	v_lshl_add_u64 v[6:7], v[2:3], 1, s[42:43]
	v_lshl_add_u64 v[8:9], v[6:7], 0, v[32:33]
	v_cvt_pk_bf16_f32 v2, v162, v163
	v_cvt_pk_bf16_f32 v3, v164, v165
	v_cvt_pk_bf16_f32 v4, v166, v167
	v_cvt_pk_bf16_f32 v5, v168, v169
	global_store_dwordx4 v[8:9], v[2:5], off nt
	v_lshl_add_u64 v[8:9], v[6:7], 0, v[30:31]
	s_nop 0
	v_cvt_pk_bf16_f32 v2, v170, v171
	v_cvt_pk_bf16_f32 v3, v172, v173
	v_cvt_pk_bf16_f32 v4, v174, v175
	v_cvt_pk_bf16_f32 v5, v176, v177
	global_store_dwordx4 v[8:9], v[2:5], off nt
	v_lshl_add_u64 v[8:9], v[6:7], 0, v[28:29]
	s_nop 0
	v_cvt_pk_bf16_f32 v2, v178, v179
	v_cvt_pk_bf16_f32 v3, v180, v181
	v_cvt_pk_bf16_f32 v4, v182, v183
	v_cvt_pk_bf16_f32 v5, v184, v185
	global_store_dwordx4 v[8:9], v[2:5], off nt
	v_lshl_add_u64 v[8:9], v[6:7], 0, v[26:27]
	s_nop 0
	v_cvt_pk_bf16_f32 v2, v186, v187
	v_cvt_pk_bf16_f32 v3, v188, v189
	v_cvt_pk_bf16_f32 v4, v190, v191
	v_cvt_pk_bf16_f32 v5, v192, v193
	global_store_dwordx4 v[8:9], v[2:5], off nt
	v_lshl_add_u64 v[8:9], v[6:7], 0, v[24:25]
	s_nop 0
	v_cvt_pk_bf16_f32 v2, v98, v99
	v_cvt_pk_bf16_f32 v3, v100, v101
	v_cvt_pk_bf16_f32 v4, v102, v103
	v_cvt_pk_bf16_f32 v5, v104, v105
	global_store_dwordx4 v[8:9], v[2:5], off nt
	v_lshl_add_u64 v[8:9], v[6:7], 0, v[22:23]
	s_nop 0
	v_cvt_pk_bf16_f32 v2, v110, v111
	v_cvt_pk_bf16_f32 v3, v112, v113
	v_cvt_pk_bf16_f32 v4, v118, v119
	v_cvt_pk_bf16_f32 v5, v120, v121
	global_store_dwordx4 v[8:9], v[2:5], off nt
	v_lshl_add_u64 v[8:9], v[6:7], 0, v[20:21]
	v_lshl_add_u64 v[6:7], v[6:7], 0, v[18:19]
	v_cvt_pk_bf16_f32 v2, v130, v131
	v_cvt_pk_bf16_f32 v3, v132, v133
	v_cvt_pk_bf16_f32 v4, v142, v143
	v_cvt_pk_bf16_f32 v5, v144, v145
	global_store_dwordx4 v[8:9], v[2:5], off nt
	s_nop 1
	v_cvt_pk_bf16_f32 v2, v150, v151
	v_cvt_pk_bf16_f32 v3, v152, v153
	v_cvt_pk_bf16_f32 v4, v154, v155
	v_cvt_pk_bf16_f32 v5, v156, v157
	global_store_dwordx4 v[6:7], v[2:5], off nt

.LBB0_303:
	s_waitcnt vmcnt(0)
	v_add_u32_e32 v10, 0x400, v240
	global_load_dwordx4 v[6:9], v10, s[14:15] offset:48
	global_load_dwordx4 v[14:17], v10, s[14:15] offset:32
	global_load_dwordx4 v[2:5], v10, s[14:15] offset:16
	s_nop 0
	global_load_dwordx4 v[10:13], v10, s[14:15]
	s_lshl_b32 s42, s31, 7
	s_ashr_i32 s43, s42, 31
	s_lshl_b64 s[42:43], s[42:43], 1
	s_add_u32 s44, s70, s42
	s_addc_u32 s45, s71, s43
	v_ashrrev_i32_e32 v19, 31, v18
	s_add_u32 s42, s72, s42
	v_lshlrev_b64 v[18:19], 1, v[18:19]
	s_addc_u32 s43, s73, s43
	v_lshl_add_u64 v[20:21], s[44:45], 0, v[18:19]
	v_lshlrev_b64 v[38:39], 1, v[228:229]
	v_lshl_add_u64 v[18:19], s[42:43], 0, v[18:19]
	v_lshl_add_u64 v[40:41], v[20:21], 0, v[38:39]
	v_cvt_pk_bf16_f32 v22, v22, v23
	v_cvt_pk_bf16_f32 v23, v24, v25
	v_cvt_pk_bf16_f32 v24, v26, v27
	v_cvt_pk_bf16_f32 v25, v28, v29
	global_store_dwordx4 v[40:41], v[22:25], off nt
	v_lshl_add_u64 v[26:27], v[18:19], 0, v[38:39]
	s_and_b64 vcc, exec, s[6:7]
	v_cvt_pk_bf16_f32 v22, v30, v31
	v_cvt_pk_bf16_f32 v23, v32, v33
	v_cvt_pk_bf16_f32 v24, v34, v35
	v_cvt_pk_bf16_f32 v25, v36, v37
	global_store_dwordx4 v[26:27], v[22:25], off nt
	v_pk_mul_f32 v[26:27], v[174:175], s[26:27] op_sel_hi:[1,0]
	v_pk_mul_f32 v[28:29], v[176:177], s[26:27] op_sel_hi:[1,0]
	v_pk_mul_f32 v[22:23], v[170:171], s[26:27] op_sel_hi:[1,0]
	v_pk_mul_f32 v[24:25], v[172:173], s[26:27] op_sel_hi:[1,0]
	s_cbranch_vccnz .LBB0_305
	v_and_b32_e32 v31, 64, v239
	v_xor_b32_e32 v30, 16, v239
	v_add_u32_e32 v31, 64, v31
	v_cmp_lt_i32_e32 vcc, v30, v31
	s_nop 1
	v_cndmask_b32_e32 v30, v239, v30, vcc
	v_lshlrev_b32_e32 v36, 2, v30
	ds_bpermute_b32 v30, v36, v22
	ds_bpermute_b32 v31, v36, v23
	s_waitcnt vmcnt(4) lgkmcnt(1)
	v_mul_f32_e32 v14, v14, v30
	v_cndmask_b32_e64 v14, v14, -v14, s[0:1]
	s_waitcnt vmcnt(2)
	v_fmac_f32_e32 v14, v22, v10
	ds_bpermute_b32 v10, v36, v24
	s_waitcnt lgkmcnt(1)
	v_mul_f32_e32 v15, v15, v31
	v_cndmask_b32_e64 v30, v22, v14, s[2:3]
	v_cndmask_b32_e64 v14, v15, -v15, s[0:1]
	v_fmac_f32_e32 v14, v23, v11
	ds_bpermute_b32 v11, v36, v25
	s_waitcnt lgkmcnt(1)
	v_mul_f32_e32 v10, v16, v10
	v_cndmask_b32_e64 v10, v10, -v10, s[0:1]
	v_fmac_f32_e32 v10, v24, v12
	v_cndmask_b32_e64 v32, v24, v10, s[2:3]
	s_waitcnt lgkmcnt(0)
	v_mul_f32_e32 v10, v17, v11
	ds_bpermute_b32 v11, v36, v26
	v_cndmask_b32_e64 v10, v10, -v10, s[0:1]
	v_fmac_f32_e32 v10, v25, v13
	v_cndmask_b32_e64 v33, v25, v10, s[2:3]
	ds_bpermute_b32 v10, v36, v27
	s_waitcnt lgkmcnt(1)
	v_mul_f32_e32 v6, v6, v11
	v_cndmask_b32_e64 v6, v6, -v6, s[0:1]
	v_fmac_f32_e32 v6, v26, v2
	v_cndmask_b32_e64 v34, v26, v6, s[2:3]
	s_waitcnt lgkmcnt(0)
	v_mul_f32_e32 v2, v7, v10
	v_cndmask_b32_e64 v2, v2, -v2, s[0:1]
	v_fmac_f32_e32 v2, v27, v3
	ds_bpermute_b32 v6, v36, v28
	v_cndmask_b32_e64 v35, v27, v2, s[2:3]
	ds_bpermute_b32 v2, v36, v29
	v_cndmask_b32_e64 v31, v23, v14, s[2:3]
	s_waitcnt lgkmcnt(1)
	v_mul_f32_e32 v3, v8, v6
	v_cndmask_b32_e64 v3, v3, -v3, s[0:1]
	s_waitcnt lgkmcnt(0)
	v_mul_f32_e32 v2, v9, v2
	v_cndmask_b32_e64 v2, v2, -v2, s[0:1]
	v_fmac_f32_e32 v3, v28, v4
	v_fmac_f32_e32 v2, v29, v5
	v_cndmask_b32_e64 v36, v28, v3, s[2:3]
	v_cndmask_b32_e64 v37, v29, v2, s[2:3]
	s_branch .LBB0_306

.LBB0_306:
	s_waitcnt vmcnt(2)
	v_add_u32_e32 v10, 0x800, v240
	global_load_dwordx4 v[6:9], v10, s[14:15] offset:48
	global_load_dwordx4 v[14:17], v10, s[14:15] offset:32
	global_load_dwordx4 v[2:5], v10, s[14:15] offset:16
	s_nop 0
	global_load_dwordx4 v[10:13], v10, s[14:15]
	v_lshlrev_b64 v[38:39], 1, v[226:227]
	v_lshl_add_u64 v[40:41], v[20:21], 0, v[38:39]
	v_cvt_pk_bf16_f32 v22, v22, v23
	v_cvt_pk_bf16_f32 v23, v24, v25
	v_cvt_pk_bf16_f32 v24, v26, v27
	v_cvt_pk_bf16_f32 v25, v28, v29
	global_store_dwordx4 v[40:41], v[22:25], off nt
	v_lshl_add_u64 v[26:27], v[18:19], 0, v[38:39]
	s_and_b64 vcc, exec, s[6:7]
	v_cvt_pk_bf16_f32 v22, v30, v31
	v_cvt_pk_bf16_f32 v23, v32, v33
	v_cvt_pk_bf16_f32 v24, v34, v35
	v_cvt_pk_bf16_f32 v25, v36, v37
	global_store_dwordx4 v[26:27], v[22:25], off nt
	v_pk_mul_f32 v[26:27], v[182:183], s[26:27] op_sel_hi:[1,0]
	v_pk_mul_f32 v[28:29], v[184:185], s[26:27] op_sel_hi:[1,0]
	v_pk_mul_f32 v[22:23], v[178:179], s[26:27] op_sel_hi:[1,0]
	v_pk_mul_f32 v[24:25], v[180:181], s[26:27] op_sel_hi:[1,0]
	s_cbranch_vccnz .LBB0_308
	v_and_b32_e32 v31, 64, v239
	v_xor_b32_e32 v30, 16, v239
	v_add_u32_e32 v31, 64, v31
	v_cmp_lt_i32_e32 vcc, v30, v31
	s_nop 1
	v_cndmask_b32_e32 v30, v239, v30, vcc
	v_lshlrev_b32_e32 v36, 2, v30
	ds_bpermute_b32 v30, v36, v22
	ds_bpermute_b32 v31, v36, v23
	s_waitcnt vmcnt(4) lgkmcnt(1)
	v_mul_f32_e32 v14, v14, v30
	v_cndmask_b32_e64 v14, v14, -v14, s[0:1]
	s_waitcnt vmcnt(2)
	v_fmac_f32_e32 v14, v22, v10
	ds_bpermute_b32 v10, v36, v24
	s_waitcnt lgkmcnt(1)
	v_mul_f32_e32 v15, v15, v31
	v_cndmask_b32_e64 v30, v22, v14, s[2:3]
	v_cndmask_b32_e64 v14, v15, -v15, s[0:1]
	v_fmac_f32_e32 v14, v23, v11
	ds_bpermute_b32 v11, v36, v25
	s_waitcnt lgkmcnt(1)
	v_mul_f32_e32 v10, v16, v10
	v_cndmask_b32_e64 v10, v10, -v10, s[0:1]
	v_fmac_f32_e32 v10, v24, v12
	v_cndmask_b32_e64 v32, v24, v10, s[2:3]
	s_waitcnt lgkmcnt(0)
	v_mul_f32_e32 v10, v17, v11
	ds_bpermute_b32 v11, v36, v26
	v_cndmask_b32_e64 v10, v10, -v10, s[0:1]
	v_fmac_f32_e32 v10, v25, v13
	v_cndmask_b32_e64 v33, v25, v10, s[2:3]
	ds_bpermute_b32 v10, v36, v27
	s_waitcnt lgkmcnt(1)
	v_mul_f32_e32 v6, v6, v11
	v_cndmask_b32_e64 v6, v6, -v6, s[0:1]
	v_fmac_f32_e32 v6, v26, v2
	v_cndmask_b32_e64 v34, v26, v6, s[2:3]
	s_waitcnt lgkmcnt(0)
	v_mul_f32_e32 v2, v7, v10
	v_cndmask_b32_e64 v2, v2, -v2, s[0:1]
	v_fmac_f32_e32 v2, v27, v3
	ds_bpermute_b32 v6, v36, v28
	v_cndmask_b32_e64 v35, v27, v2, s[2:3]
	ds_bpermute_b32 v2, v36, v29
	v_cndmask_b32_e64 v31, v23, v14, s[2:3]
	s_waitcnt lgkmcnt(1)
	v_mul_f32_e32 v3, v8, v6
	v_cndmask_b32_e64 v3, v3, -v3, s[0:1]
	s_waitcnt lgkmcnt(0)
	v_mul_f32_e32 v2, v9, v2
	v_cndmask_b32_e64 v2, v2, -v2, s[0:1]
	v_fmac_f32_e32 v3, v28, v4
	v_fmac_f32_e32 v2, v29, v5
	v_cndmask_b32_e64 v36, v28, v3, s[2:3]
	v_cndmask_b32_e64 v37, v29, v2, s[2:3]
	s_branch .LBB0_309

.LBB0_309:
	s_waitcnt vmcnt(2)
	v_add_u32_e32 v10, 0xc00, v240
	global_load_dwordx4 v[6:9], v10, s[14:15] offset:48
	global_load_dwordx4 v[14:17], v10, s[14:15] offset:32
	global_load_dwordx4 v[2:5], v10, s[14:15] offset:16
	s_nop 0
	global_load_dwordx4 v[10:13], v10, s[14:15]
	v_lshlrev_b64 v[38:39], 1, v[224:225]
	v_lshl_add_u64 v[40:41], v[20:21], 0, v[38:39]
	v_cvt_pk_bf16_f32 v22, v22, v23
	v_cvt_pk_bf16_f32 v23, v24, v25
	v_cvt_pk_bf16_f32 v24, v26, v27
	v_cvt_pk_bf16_f32 v25, v28, v29
	global_store_dwordx4 v[40:41], v[22:25], off nt
	v_lshl_add_u64 v[26:27], v[18:19], 0, v[38:39]
	s_and_b64 vcc, exec, s[6:7]
	v_cvt_pk_bf16_f32 v22, v30, v31
	v_cvt_pk_bf16_f32 v23, v32, v33
	v_cvt_pk_bf16_f32 v24, v34, v35
	v_cvt_pk_bf16_f32 v25, v36, v37
	global_store_dwordx4 v[26:27], v[22:25], off nt
	v_pk_mul_f32 v[26:27], v[190:191], s[26:27] op_sel_hi:[1,0]
	v_pk_mul_f32 v[28:29], v[192:193], s[26:27] op_sel_hi:[1,0]
	v_pk_mul_f32 v[22:23], v[186:187], s[26:27] op_sel_hi:[1,0]
	v_pk_mul_f32 v[24:25], v[188:189], s[26:27] op_sel_hi:[1,0]
	s_cbranch_vccnz .LBB0_311
	v_and_b32_e32 v31, 64, v239
	v_xor_b32_e32 v30, 16, v239
	v_add_u32_e32 v31, 64, v31
	v_cmp_lt_i32_e32 vcc, v30, v31
	s_nop 1
	v_cndmask_b32_e32 v30, v239, v30, vcc
	v_lshlrev_b32_e32 v36, 2, v30
	ds_bpermute_b32 v30, v36, v22
	ds_bpermute_b32 v31, v36, v23
	s_waitcnt vmcnt(4) lgkmcnt(1)
	v_mul_f32_e32 v14, v14, v30
	v_cndmask_b32_e64 v14, v14, -v14, s[0:1]
	s_waitcnt vmcnt(2)
	v_fmac_f32_e32 v14, v22, v10
	ds_bpermute_b32 v10, v36, v24
	s_waitcnt lgkmcnt(1)
	v_mul_f32_e32 v15, v15, v31
	v_cndmask_b32_e64 v30, v22, v14, s[2:3]
	v_cndmask_b32_e64 v14, v15, -v15, s[0:1]
	v_fmac_f32_e32 v14, v23, v11
	ds_bpermute_b32 v11, v36, v25
	s_waitcnt lgkmcnt(1)
	v_mul_f32_e32 v10, v16, v10
	v_cndmask_b32_e64 v10, v10, -v10, s[0:1]
	v_fmac_f32_e32 v10, v24, v12
	v_cndmask_b32_e64 v32, v24, v10, s[2:3]
	s_waitcnt lgkmcnt(0)
	v_mul_f32_e32 v10, v17, v11
	ds_bpermute_b32 v11, v36, v26
	v_cndmask_b32_e64 v10, v10, -v10, s[0:1]
	v_fmac_f32_e32 v10, v25, v13
	v_cndmask_b32_e64 v33, v25, v10, s[2:3]
	ds_bpermute_b32 v10, v36, v27
	s_waitcnt lgkmcnt(1)
	v_mul_f32_e32 v6, v6, v11
	v_cndmask_b32_e64 v6, v6, -v6, s[0:1]
	v_fmac_f32_e32 v6, v26, v2
	v_cndmask_b32_e64 v34, v26, v6, s[2:3]
	s_waitcnt lgkmcnt(0)
	v_mul_f32_e32 v2, v7, v10
	v_cndmask_b32_e64 v2, v2, -v2, s[0:1]
	v_fmac_f32_e32 v2, v27, v3
	ds_bpermute_b32 v6, v36, v28
	v_cndmask_b32_e64 v35, v27, v2, s[2:3]
	ds_bpermute_b32 v2, v36, v29
	v_cndmask_b32_e64 v31, v23, v14, s[2:3]
	s_waitcnt lgkmcnt(1)
	v_mul_f32_e32 v3, v8, v6
	v_cndmask_b32_e64 v3, v3, -v3, s[0:1]
	s_waitcnt lgkmcnt(0)
	v_mul_f32_e32 v2, v9, v2
	v_cndmask_b32_e64 v2, v2, -v2, s[0:1]
	v_fmac_f32_e32 v3, v28, v4
	v_fmac_f32_e32 v2, v29, v5
	v_cndmask_b32_e64 v36, v28, v3, s[2:3]
	v_cndmask_b32_e64 v37, v29, v2, s[2:3]
	s_branch .LBB0_312

.LBB0_312:
	s_waitcnt vmcnt(2)
	v_add_u32_e32 v10, 0x2000, v240
	global_load_dwordx4 v[6:9], v10, s[14:15] offset:48
	global_load_dwordx4 v[14:17], v10, s[14:15] offset:32
	global_load_dwordx4 v[2:5], v10, s[14:15] offset:16
	s_nop 0
	global_load_dwordx4 v[10:13], v10, s[14:15]
	v_lshlrev_b64 v[38:39], 1, v[222:223]
	v_lshl_add_u64 v[40:41], v[20:21], 0, v[38:39]
	v_cvt_pk_bf16_f32 v22, v22, v23
	v_cvt_pk_bf16_f32 v23, v24, v25
	v_cvt_pk_bf16_f32 v24, v26, v27
	v_cvt_pk_bf16_f32 v25, v28, v29
	global_store_dwordx4 v[40:41], v[22:25], off nt
	v_lshl_add_u64 v[26:27], v[18:19], 0, v[38:39]
	s_and_b64 vcc, exec, s[6:7]
	v_cvt_pk_bf16_f32 v22, v30, v31
	v_cvt_pk_bf16_f32 v23, v32, v33
	v_cvt_pk_bf16_f32 v24, v34, v35
	v_cvt_pk_bf16_f32 v25, v36, v37
	global_store_dwordx4 v[26:27], v[22:25], off nt
	v_pk_mul_f32 v[26:27], v[102:103], s[26:27] op_sel_hi:[1,0]
	v_pk_mul_f32 v[28:29], v[104:105], s[26:27] op_sel_hi:[1,0]
	v_pk_mul_f32 v[22:23], v[98:99], s[26:27] op_sel_hi:[1,0]
	v_pk_mul_f32 v[24:25], v[100:101], s[26:27] op_sel_hi:[1,0]
	s_cbranch_vccnz .LBB0_314
	v_and_b32_e32 v31, 64, v239
	v_xor_b32_e32 v30, 16, v239
	v_add_u32_e32 v31, 64, v31
	v_cmp_lt_i32_e32 vcc, v30, v31
	s_nop 1
	v_cndmask_b32_e32 v30, v239, v30, vcc
	v_lshlrev_b32_e32 v36, 2, v30
	ds_bpermute_b32 v30, v36, v22
	ds_bpermute_b32 v31, v36, v23
	s_waitcnt vmcnt(4) lgkmcnt(1)
	v_mul_f32_e32 v14, v14, v30
	v_cndmask_b32_e64 v14, v14, -v14, s[0:1]
	s_waitcnt vmcnt(2)
	v_fmac_f32_e32 v14, v22, v10
	ds_bpermute_b32 v10, v36, v24
	s_waitcnt lgkmcnt(1)
	v_mul_f32_e32 v15, v15, v31
	v_cndmask_b32_e64 v30, v22, v14, s[2:3]
	v_cndmask_b32_e64 v14, v15, -v15, s[0:1]
	v_fmac_f32_e32 v14, v23, v11
	ds_bpermute_b32 v11, v36, v25
	s_waitcnt lgkmcnt(1)
	v_mul_f32_e32 v10, v16, v10
	v_cndmask_b32_e64 v10, v10, -v10, s[0:1]
	v_fmac_f32_e32 v10, v24, v12
	v_cndmask_b32_e64 v32, v24, v10, s[2:3]
	s_waitcnt lgkmcnt(0)
	v_mul_f32_e32 v10, v17, v11
	ds_bpermute_b32 v11, v36, v26
	v_cndmask_b32_e64 v10, v10, -v10, s[0:1]
	v_fmac_f32_e32 v10, v25, v13
	v_cndmask_b32_e64 v33, v25, v10, s[2:3]
	ds_bpermute_b32 v10, v36, v27
	s_waitcnt lgkmcnt(1)
	v_mul_f32_e32 v6, v6, v11
	v_cndmask_b32_e64 v6, v6, -v6, s[0:1]
	v_fmac_f32_e32 v6, v26, v2
	v_cndmask_b32_e64 v34, v26, v6, s[2:3]
	s_waitcnt lgkmcnt(0)
	v_mul_f32_e32 v2, v7, v10
	v_cndmask_b32_e64 v2, v2, -v2, s[0:1]
	v_fmac_f32_e32 v2, v27, v3
	ds_bpermute_b32 v6, v36, v28
	v_cndmask_b32_e64 v35, v27, v2, s[2:3]
	ds_bpermute_b32 v2, v36, v29
	v_cndmask_b32_e64 v31, v23, v14, s[2:3]
	s_waitcnt lgkmcnt(1)
	v_mul_f32_e32 v3, v8, v6
	v_cndmask_b32_e64 v3, v3, -v3, s[0:1]
	s_waitcnt lgkmcnt(0)
	v_mul_f32_e32 v2, v9, v2
	v_cndmask_b32_e64 v2, v2, -v2, s[0:1]
	v_fmac_f32_e32 v3, v28, v4
	v_fmac_f32_e32 v2, v29, v5
	v_cndmask_b32_e64 v36, v28, v3, s[2:3]
	v_cndmask_b32_e64 v37, v29, v2, s[2:3]
	s_branch .LBB0_315

.LBB0_315:
	s_waitcnt vmcnt(2)
	v_add_u32_e32 v10, 0x2400, v240
	global_load_dwordx4 v[6:9], v10, s[14:15] offset:48
	global_load_dwordx4 v[14:17], v10, s[14:15] offset:32
	global_load_dwordx4 v[2:5], v10, s[14:15] offset:16
	s_nop 0
	global_load_dwordx4 v[10:13], v10, s[14:15]
	v_lshlrev_b64 v[38:39], 1, v[212:213]
	v_lshl_add_u64 v[40:41], v[20:21], 0, v[38:39]
	v_cvt_pk_bf16_f32 v22, v22, v23
	v_cvt_pk_bf16_f32 v23, v24, v25
	v_cvt_pk_bf16_f32 v24, v26, v27
	v_cvt_pk_bf16_f32 v25, v28, v29
	global_store_dwordx4 v[40:41], v[22:25], off nt
	v_lshl_add_u64 v[26:27], v[18:19], 0, v[38:39]
	s_and_b64 vcc, exec, s[6:7]
	v_cvt_pk_bf16_f32 v22, v30, v31
	v_cvt_pk_bf16_f32 v23, v32, v33
	v_cvt_pk_bf16_f32 v24, v34, v35
	v_cvt_pk_bf16_f32 v25, v36, v37
	global_store_dwordx4 v[26:27], v[22:25], off nt
	v_pk_mul_f32 v[26:27], v[118:119], s[26:27] op_sel_hi:[1,0]
	v_pk_mul_f32 v[28:29], v[120:121], s[26:27] op_sel_hi:[1,0]
	v_pk_mul_f32 v[22:23], v[110:111], s[26:27] op_sel_hi:[1,0]
	v_pk_mul_f32 v[24:25], v[112:113], s[26:27] op_sel_hi:[1,0]
	s_cbranch_vccnz .LBB0_317
	v_and_b32_e32 v31, 64, v239
	v_xor_b32_e32 v30, 16, v239
	v_add_u32_e32 v31, 64, v31
	v_cmp_lt_i32_e32 vcc, v30, v31
	s_nop 1
	v_cndmask_b32_e32 v30, v239, v30, vcc
	v_lshlrev_b32_e32 v36, 2, v30
	ds_bpermute_b32 v30, v36, v22
	ds_bpermute_b32 v31, v36, v23
	s_waitcnt vmcnt(4) lgkmcnt(1)
	v_mul_f32_e32 v14, v14, v30
	v_cndmask_b32_e64 v14, v14, -v14, s[0:1]
	s_waitcnt vmcnt(2)
	v_fmac_f32_e32 v14, v22, v10
	ds_bpermute_b32 v10, v36, v24
	s_waitcnt lgkmcnt(1)
	v_mul_f32_e32 v15, v15, v31
	v_cndmask_b32_e64 v30, v22, v14, s[2:3]
	v_cndmask_b32_e64 v14, v15, -v15, s[0:1]
	v_fmac_f32_e32 v14, v23, v11
	ds_bpermute_b32 v11, v36, v25
	s_waitcnt lgkmcnt(1)
	v_mul_f32_e32 v10, v16, v10
	v_cndmask_b32_e64 v10, v10, -v10, s[0:1]
	v_fmac_f32_e32 v10, v24, v12
	v_cndmask_b32_e64 v32, v24, v10, s[2:3]
	s_waitcnt lgkmcnt(0)
	v_mul_f32_e32 v10, v17, v11
	ds_bpermute_b32 v11, v36, v26
	v_cndmask_b32_e64 v10, v10, -v10, s[0:1]
	v_fmac_f32_e32 v10, v25, v13
	v_cndmask_b32_e64 v33, v25, v10, s[2:3]
	ds_bpermute_b32 v10, v36, v27
	s_waitcnt lgkmcnt(1)
	v_mul_f32_e32 v6, v6, v11
	v_cndmask_b32_e64 v6, v6, -v6, s[0:1]
	v_fmac_f32_e32 v6, v26, v2
	v_cndmask_b32_e64 v34, v26, v6, s[2:3]
	s_waitcnt lgkmcnt(0)
	v_mul_f32_e32 v2, v7, v10
	v_cndmask_b32_e64 v2, v2, -v2, s[0:1]
	v_fmac_f32_e32 v2, v27, v3
	ds_bpermute_b32 v6, v36, v28
	v_cndmask_b32_e64 v35, v27, v2, s[2:3]
	ds_bpermute_b32 v2, v36, v29
	v_cndmask_b32_e64 v31, v23, v14, s[2:3]
	s_waitcnt lgkmcnt(1)
	v_mul_f32_e32 v3, v8, v6
	v_cndmask_b32_e64 v3, v3, -v3, s[0:1]
	s_waitcnt lgkmcnt(0)
	v_mul_f32_e32 v2, v9, v2
	v_cndmask_b32_e64 v2, v2, -v2, s[0:1]
	v_fmac_f32_e32 v3, v28, v4
	v_fmac_f32_e32 v2, v29, v5
	v_cndmask_b32_e64 v36, v28, v3, s[2:3]
	v_cndmask_b32_e64 v37, v29, v2, s[2:3]
	s_branch .LBB0_318

.LBB0_318:
	s_waitcnt vmcnt(2)
	v_add_u32_e32 v10, 0x2800, v240
	global_load_dwordx4 v[6:9], v10, s[14:15] offset:48
	global_load_dwordx4 v[14:17], v10, s[14:15] offset:32
	global_load_dwordx4 v[2:5], v10, s[14:15] offset:16
	s_nop 0
	global_load_dwordx4 v[10:13], v10, s[14:15]
	v_lshlrev_b64 v[38:39], 1, v[210:211]
	v_lshl_add_u64 v[40:41], v[20:21], 0, v[38:39]
	v_cvt_pk_bf16_f32 v22, v22, v23
	v_cvt_pk_bf16_f32 v23, v24, v25
	v_cvt_pk_bf16_f32 v24, v26, v27
	v_cvt_pk_bf16_f32 v25, v28, v29
	global_store_dwordx4 v[40:41], v[22:25], off nt
	v_lshl_add_u64 v[26:27], v[18:19], 0, v[38:39]
	s_and_b64 vcc, exec, s[6:7]
	v_cvt_pk_bf16_f32 v22, v30, v31
	v_cvt_pk_bf16_f32 v23, v32, v33
	v_cvt_pk_bf16_f32 v24, v34, v35
	v_cvt_pk_bf16_f32 v25, v36, v37
	global_store_dwordx4 v[26:27], v[22:25], off nt
	v_pk_mul_f32 v[26:27], v[142:143], s[26:27] op_sel_hi:[1,0]
	v_pk_mul_f32 v[28:29], v[144:145], s[26:27] op_sel_hi:[1,0]
	v_pk_mul_f32 v[22:23], v[130:131], s[26:27] op_sel_hi:[1,0]
	v_pk_mul_f32 v[24:25], v[132:133], s[26:27] op_sel_hi:[1,0]
	s_cbranch_vccnz .LBB0_320
	v_and_b32_e32 v31, 64, v239
	v_xor_b32_e32 v30, 16, v239
	v_add_u32_e32 v31, 64, v31
	v_cmp_lt_i32_e32 vcc, v30, v31
	s_nop 1
	v_cndmask_b32_e32 v30, v239, v30, vcc
	v_lshlrev_b32_e32 v36, 2, v30
	ds_bpermute_b32 v30, v36, v22
	ds_bpermute_b32 v31, v36, v23
	s_waitcnt vmcnt(4) lgkmcnt(1)
	v_mul_f32_e32 v14, v14, v30
	v_cndmask_b32_e64 v14, v14, -v14, s[0:1]
	s_waitcnt vmcnt(2)
	v_fmac_f32_e32 v14, v22, v10
	ds_bpermute_b32 v10, v36, v24
	s_waitcnt lgkmcnt(1)
	v_mul_f32_e32 v15, v15, v31
	v_cndmask_b32_e64 v30, v22, v14, s[2:3]
	v_cndmask_b32_e64 v14, v15, -v15, s[0:1]
	v_fmac_f32_e32 v14, v23, v11
	ds_bpermute_b32 v11, v36, v25
	s_waitcnt lgkmcnt(1)
	v_mul_f32_e32 v10, v16, v10
	v_cndmask_b32_e64 v10, v10, -v10, s[0:1]
	v_fmac_f32_e32 v10, v24, v12
	v_cndmask_b32_e64 v32, v24, v10, s[2:3]
	s_waitcnt lgkmcnt(0)
	v_mul_f32_e32 v10, v17, v11
	ds_bpermute_b32 v11, v36, v26
	v_cndmask_b32_e64 v10, v10, -v10, s[0:1]
	v_fmac_f32_e32 v10, v25, v13
	v_cndmask_b32_e64 v33, v25, v10, s[2:3]
	ds_bpermute_b32 v10, v36, v27
	s_waitcnt lgkmcnt(1)
	v_mul_f32_e32 v6, v6, v11
	v_cndmask_b32_e64 v6, v6, -v6, s[0:1]
	v_fmac_f32_e32 v6, v26, v2
	v_cndmask_b32_e64 v34, v26, v6, s[2:3]
	s_waitcnt lgkmcnt(0)
	v_mul_f32_e32 v2, v7, v10
	v_cndmask_b32_e64 v2, v2, -v2, s[0:1]
	v_fmac_f32_e32 v2, v27, v3
	ds_bpermute_b32 v6, v36, v28
	v_cndmask_b32_e64 v35, v27, v2, s[2:3]
	ds_bpermute_b32 v2, v36, v29
	v_cndmask_b32_e64 v31, v23, v14, s[2:3]
	s_waitcnt lgkmcnt(1)
	v_mul_f32_e32 v3, v8, v6
	v_cndmask_b32_e64 v3, v3, -v3, s[0:1]
	s_waitcnt lgkmcnt(0)
	v_mul_f32_e32 v2, v9, v2
	v_cndmask_b32_e64 v2, v2, -v2, s[0:1]
	v_fmac_f32_e32 v3, v28, v4
	v_fmac_f32_e32 v2, v29, v5
	v_cndmask_b32_e64 v36, v28, v3, s[2:3]
	v_cndmask_b32_e64 v37, v29, v2, s[2:3]
	s_branch .LBB0_321

.LBB0_321:
	s_waitcnt vmcnt(2)
	v_add_u32_e32 v10, 0x2c00, v240
	global_load_dwordx4 v[6:9], v10, s[14:15] offset:48
	global_load_dwordx4 v[14:17], v10, s[14:15] offset:32
	global_load_dwordx4 v[2:5], v10, s[14:15] offset:16
	s_nop 0
	global_load_dwordx4 v[10:13], v10, s[14:15]
	v_lshlrev_b64 v[38:39], 1, v[208:209]
	v_lshl_add_u64 v[40:41], v[20:21], 0, v[38:39]
	v_cvt_pk_bf16_f32 v22, v22, v23
	v_cvt_pk_bf16_f32 v23, v24, v25
	v_cvt_pk_bf16_f32 v24, v26, v27
	v_cvt_pk_bf16_f32 v25, v28, v29
	global_store_dwordx4 v[40:41], v[22:25], off nt
	v_lshl_add_u64 v[26:27], v[18:19], 0, v[38:39]
	s_and_b64 vcc, exec, s[6:7]
	v_cvt_pk_bf16_f32 v22, v30, v31
	v_cvt_pk_bf16_f32 v23, v32, v33
	v_cvt_pk_bf16_f32 v24, v34, v35
	v_cvt_pk_bf16_f32 v25, v36, v37
	global_store_dwordx4 v[26:27], v[22:25], off nt
	v_pk_mul_f32 v[26:27], v[154:155], s[26:27] op_sel_hi:[1,0]
	v_pk_mul_f32 v[28:29], v[156:157], s[26:27] op_sel_hi:[1,0]
	v_pk_mul_f32 v[22:23], v[150:151], s[26:27] op_sel_hi:[1,0]
	v_pk_mul_f32 v[24:25], v[152:153], s[26:27] op_sel_hi:[1,0]
	s_cbranch_vccnz .LBB0_323
	v_and_b32_e32 v31, 64, v239
	v_xor_b32_e32 v30, 16, v239
	v_add_u32_e32 v31, 64, v31
	v_cmp_lt_i32_e32 vcc, v30, v31
	s_nop 1
	v_cndmask_b32_e32 v30, v239, v30, vcc
	v_lshlrev_b32_e32 v30, 2, v30
	ds_bpermute_b32 v31, v30, v22
	ds_bpermute_b32 v32, v30, v23
	s_waitcnt vmcnt(4) lgkmcnt(1)
	v_mul_f32_e32 v14, v14, v31
	v_cndmask_b32_e64 v14, v14, -v14, s[0:1]
	s_waitcnt vmcnt(2)
	v_fmac_f32_e32 v14, v22, v10
	s_waitcnt lgkmcnt(0)
	v_mul_f32_e32 v15, v15, v32
	v_cndmask_b32_e64 v10, v22, v14, s[2:3]
	ds_bpermute_b32 v14, v30, v24
	v_cndmask_b32_e64 v15, v15, -v15, s[0:1]
	v_fmac_f32_e32 v15, v23, v11
	v_cndmask_b32_e64 v11, v23, v15, s[2:3]
	ds_bpermute_b32 v15, v30, v25
	s_waitcnt lgkmcnt(1)
	v_mul_f32_e32 v14, v16, v14
	v_cndmask_b32_e64 v14, v14, -v14, s[0:1]
	v_fmac_f32_e32 v14, v24, v12
	v_cndmask_b32_e64 v12, v24, v14, s[2:3]
	s_waitcnt lgkmcnt(0)
	v_mul_f32_e32 v14, v17, v15
	ds_bpermute_b32 v15, v30, v26
	v_cndmask_b32_e64 v14, v14, -v14, s[0:1]
	v_fmac_f32_e32 v14, v25, v13
	v_cndmask_b32_e64 v13, v25, v14, s[2:3]
	ds_bpermute_b32 v14, v30, v27
	s_waitcnt lgkmcnt(1)
	v_mul_f32_e32 v6, v6, v15
	v_cndmask_b32_e64 v6, v6, -v6, s[0:1]
	v_fmac_f32_e32 v6, v26, v2
	v_cndmask_b32_e64 v2, v26, v6, s[2:3]
	s_waitcnt lgkmcnt(0)
	v_mul_f32_e32 v6, v7, v14
	v_cndmask_b32_e64 v6, v6, -v6, s[0:1]
	v_fmac_f32_e32 v6, v27, v3
	ds_bpermute_b32 v7, v30, v28
	v_cndmask_b32_e64 v3, v27, v6, s[2:3]
	ds_bpermute_b32 v6, v30, v29
	s_waitcnt lgkmcnt(1)
	v_mul_f32_e32 v7, v8, v7
	v_cndmask_b32_e64 v7, v7, -v7, s[0:1]
	s_waitcnt lgkmcnt(0)
	v_mul_f32_e32 v6, v9, v6
	v_cndmask_b32_e64 v6, v6, -v6, s[0:1]
	v_fmac_f32_e32 v7, v28, v4
	v_fmac_f32_e32 v6, v29, v5
	v_cndmask_b32_e64 v4, v28, v7, s[2:3]
	v_cndmask_b32_e64 v5, v29, v6, s[2:3]
	s_branch .LBB0_324

.LBB0_324:
	v_lshlrev_b64 v[14:15], 1, v[206:207]
	v_lshl_add_u64 v[16:17], v[20:21], 0, v[14:15]
	v_cvt_pk_bf16_f32 v6, v22, v23
	v_cvt_pk_bf16_f32 v7, v24, v25
	v_cvt_pk_bf16_f32 v8, v26, v27
	v_cvt_pk_bf16_f32 v9, v28, v29
	global_store_dwordx4 v[16:17], v[6:9], off nt
	v_lshl_add_u64 v[14:15], v[18:19], 0, v[14:15]
	s_nop 0
	v_cvt_pk_bf16_f32 v6, v10, v11
	v_cvt_pk_bf16_f32 v7, v12, v13
	v_cvt_pk_bf16_f32 v8, v2, v3
	v_cvt_pk_bf16_f32 v9, v4, v5
	global_store_dwordx4 v[14:15], v[6:9], off nt
	s_andn2_b64 vcc, exec, s[38:39]
	s_mov_b64 s[6:7], -1
	s_cbranch_vccnz .LBB0_158
